# P4/P14 output-projection epilogues rewritten by hand: residual loads issued up front (P14 all 8 groups, P4 5+3), counted vmcnt waits, no header drain
# speedup vs baseline: 1.0090x; 1.0032x over previous
; #define PG8_STAGE(bufoff, gbase, voff) do { _Pragma("unroll") for (int _i = 0; _i < 2; ++_i) \
;         __builtin_amdgcn_global_load_lds((const unsigned*)((const char*)(gbase) + (voff)[_i]), (PG8_LAS unsigned*)(lds + (bufoff) + ldsw + _i * 8192), 16, 0, 0); } while (0)
; #define PG8_STAGE_A(bufoff, gbase, h, nx) do { if constexpr (Sched::GATHER) { const unsigned vv_[2] = {(nx) ? vAn[h][0] : vA[h][0], (nx) ? vAn[h][1] : vA[h][1]}; PG8_STAGE(bufoff, gbase, vv_); } \
;         else { PG8_STAGE(bufoff, (gbase) + (h) * hstep, voffA); } } while (0)
; #define PG8_LDA(dst, b, h) do { _Pragma("unroll") for (int m = 0; m < 4; ++m) _Pragma("unroll") for (int k = 0; k < 2; ++k) dst[m][k] = *(const PG8_LAS bf16x8*)(lds + PG8_SA(b, h) + aoff + m * 2048 + k * 1024); } while (0)
; #define PG8_WAIT_V(n) asm volatile("s_waitcnt vmcnt(" #n ")" ::: "memory")
; #define PG8_WAIT_L(n) asm volatile("s_waitcnt lgkmcnt(" #n ")" ::: "memory")
;     ...
;         const bool has_next = S.next(ui + 1, nxt);
;         const char* nA = Sched::GATHER ? cA : (has_next ? (const char*)g.A + (size_t)nxt.pm * tstep : cA);
;         if constexpr (Sched::GATHER) { if (has_next) { PG8_AOFF(vAn, ui + 1); } else { _Pragma("unroll") for (int h_ = 0; h_ < 2; ++h_) _Pragma("unroll") for (int i_ = 0; i_ < 2; ++i_) vAn[h_][i_] = vA[h_][i_]; } } const char* nB = has_next ? (const char*)g.Bt + (size_t)nxt.pb * tstep : cB;
; #pragma nounroll
;         for (int t = 0; t < nt; t += 2) {
;             const bool last = (t == nt - 2);
;             const char* a1 = cA + (size_t)(t + 1) * kstep;
;             const char* a2 = last ? nA : cA + (size_t)(t + 2) * kstep; const char* b2 = last ? nB : cB + (size_t)(t + 2) * kstep;
;             const char* a3 = a2 + kstep; const char* b3 = b2 + kstep;
;             if (last && has_next) S.a_ready(nxt);
;             if constexpr (SP2) {
;             PG8_LDB(B0, 0, 0); PG8_LDB(B1, 0, 1); PG8_SCHED; PG8_LDA(At, 0, 0); PG8_STAGE_A(PG8_SA(1, 1), a1, 1, false);
;             PG8_WAIT_V(8); PG8_WAIT_L(0); PG8_BAR; PG8_MMA(0, 0, At, B0); PG8_MMA(0, 1, At, B1); PG8_BAR; PG8_SCHED;
;             PG8_LDA(At, 0, 1); PG8_STAGE(PG8_SB(0, 0), b2, voffB); PG8_STAGE(PG8_SB(0, 1), b2 + hstepB, voffB); PG8_STAGE_A(PG8_SA(0, 0), a2, 0, last);
;             PG8_WAIT_V(8); PG8_WAIT_L(0); PG8_BAR; PG8_MMA(1, 0, At, B0); PG8_MMA(1, 1, At, B1); PG8_BAR; PG8_SCHED;
.LBB0_473:
	s_ashr_i32 s15, s14, 31
	s_lshl_b64 s[16:17], s[14:15], 18
	v_readlane_b32 s18, v255, 21
	v_readlane_b32 s19, v255, 22
	s_add_u32 s16, s18, s16
	s_addc_u32 s17, s19, s17
	s_and_b64 s[18:19], s[2:3], exec
	s_cselect_b32 s1, s17, s23
	s_cselect_b32 s15, s16, s22
	s_ashr_i32 s13, s12, 31
	s_lshl_b64 s[18:19], s[12:13], 18
	v_readlane_b32 s26, v254, 53
	v_readlane_b32 s27, v254, 54
	s_add_u32 s18, s26, s18
	s_addc_u32 s19, s27, s19
	s_and_b64 s[26:27], s[2:3], exec
	s_cselect_b32 s13, s19, s25
	s_cselect_b32 s21, s18, s24
	s_add_u32 s22, s22, 0x20080
	s_addc_u32 s23, s23, 0
	s_add_u32 s33, s24, 0x100
	s_addc_u32 s42, s25, 0
	s_mov_b32 s43, -2
	ds_read_b128 v[26:29], v188
	ds_read_b128 v[30:33], v188 offset:1024
	ds_read_b128 v[18:21], v188 offset:2048
	ds_read_b128 v[22:25], v188 offset:3072
	ds_read_b128 v[10:13], v189
	ds_read_b128 v[14:17], v189 offset:1024
	ds_read_b128 v[2:5], v189 offset:2048
	ds_read_b128 v[6:9], v189 offset:3072
	s_add_u32 s24, s22, 0xfffe0080
	s_addc_u32 s25, s23, -1
	s_cmp_eq_u32 s43, 4
	s_cselect_b32 s27, s1, s25
	s_cselect_b32 s26, s15, s24
	s_cselect_b32 s25, s13, s42
	s_cselect_b32 s24, s21, s33
	v_lshl_add_u64 v[218:219], s[22:23], 0, v[170:171]
	s_add_i32 m0, s30, 0xc000
	ds_read_b128 v[178:181], v190
	ds_read_b128 v[182:185], v190 offset:1024
	ds_read_b128 v[194:197], v190 offset:2048
	ds_read_b128 v[198:201], v190 offset:3072
	ds_read_b128 v[202:205], v190 offset:4096
	ds_read_b128 v[206:209], v190 offset:5120
	ds_read_b128 v[210:213], v190 offset:6144
	ds_read_b128 v[214:217], v190 offset:7168
	global_load_lds_dwordx4 v[218:219], off
	v_lshl_add_u64 v[218:219], s[22:23], 0, v[172:173]
	s_add_i32 m0, s30, 0xe000
	s_nop 0
	global_load_lds_dwordx4 v[218:219], off
	s_waitcnt vmcnt(8)
	s_waitcnt lgkmcnt(0)
	s_barrier
	s_setprio 1
	s_nop 3
	s_waitcnt lgkmcnt(0)
	v_mfma_scale_f32_16x16x128_f8f6f4 v[158:161], v[26:33], v[178:185], 0, v191, v192 op_sel_hi:[0,0,0]
	v_mfma_scale_f32_16x16x128_f8f6f4 v[154:157], v[18:25], v[178:185], 0, v191, v192 op_sel_hi:[0,0,0]
	v_mfma_scale_f32_16x16x128_f8f6f4 v[142:145], v[26:33], v[194:201], 0, v191, v192 op_sel_hi:[0,0,0]
	v_mfma_scale_f32_16x16x128_f8f6f4 v[138:141], v[18:25], v[194:201], 0, v191, v192 op_sel_hi:[0,0,0]
	v_mfma_scale_f32_16x16x128_f8f6f4 v[126:129], v[26:33], v[202:209], 0, v191, v192 op_sel_hi:[0,0,0]
	v_mfma_scale_f32_16x16x128_f8f6f4 v[122:125], v[18:25], v[202:209], 0, v191, v192 op_sel_hi:[0,0,0]
	v_mfma_scale_f32_16x16x128_f8f6f4 v[110:113], v[26:33], v[210:217], 0, v191, v192 op_sel_hi:[0,0,0]
	v_mfma_scale_f32_16x16x128_f8f6f4 v[106:109], v[18:25], v[210:217], 0, v191, v192 op_sel_hi:[0,0,0]
	s_setprio 0
	s_setprio 1
	s_nop 3
	v_mfma_scale_f32_16x16x128_f8f6f4 v[150:153], v[10:17], v[178:185], 0, v191, v192 op_sel_hi:[0,0,0]
	v_mfma_scale_f32_16x16x128_f8f6f4 v[146:149], v[2:9], v[178:185], 0, v191, v192 op_sel_hi:[0,0,0]
	v_mfma_scale_f32_16x16x128_f8f6f4 v[134:137], v[10:17], v[194:201], 0, v191, v192 op_sel_hi:[0,0,0]
	v_mfma_scale_f32_16x16x128_f8f6f4 v[130:133], v[2:9], v[194:201], 0, v191, v192 op_sel_hi:[0,0,0]
	v_mfma_scale_f32_16x16x128_f8f6f4 v[118:121], v[10:17], v[202:209], 0, v191, v192 op_sel_hi:[0,0,0]
	v_mfma_scale_f32_16x16x128_f8f6f4 v[114:117], v[2:9], v[202:209], 0, v191, v192 op_sel_hi:[0,0,0]
	v_mfma_scale_f32_16x16x128_f8f6f4 v[102:105], v[10:17], v[210:217], 0, v191, v192 op_sel_hi:[0,0,0]
	v_mfma_scale_f32_16x16x128_f8f6f4 v[98:101], v[2:9], v[210:217], 0, v191, v192 op_sel_hi:[0,0,0]
	s_setprio 0
	s_barrier
	s_add_i32 s44, s40, s28
	v_lshl_add_u64 v[178:179], s[24:25], 0, v[164:165]
	s_mov_b32 m0, s44
	ds_read_b128 v[194:197], v190 offset:16384
	ds_read_b128 v[198:201], v190 offset:17408
	ds_read_b128 v[202:205], v190 offset:18432
	ds_read_b128 v[206:209], v190 offset:19456
	ds_read_b128 v[210:213], v190 offset:20480
	ds_read_b128 v[214:217], v190 offset:21504
	ds_read_b128 v[218:221], v190 offset:22528
	ds_read_b128 v[222:225], v190 offset:23552
	global_load_lds_dwordx4 v[178:179], off
	s_add_i32 m0, s44, 0x2000
	s_add_u32 s44, s24, 0x2000
	v_lshl_add_u64 v[180:181], s[24:25], 0, v[168:169]
	s_addc_u32 s45, s25, 0
	s_add_i32 s46, s41, s28
	global_load_lds_dwordx4 v[180:181], off
	v_lshl_add_u64 v[182:183], s[44:45], 0, v[164:165]
	s_mov_b32 m0, s46
	v_lshl_add_u64 v[184:185], s[26:27], 0, v[166:167]
	global_load_lds_dwordx4 v[182:183], off
	v_lshl_add_u64 v[182:183], s[44:45], 0, v[168:169]
	s_add_i32 m0, s46, 0x2000
	s_nop 0
	global_load_lds_dwordx4 v[182:183], off
	v_lshl_add_u64 v[182:183], s[26:27], 0, v[162:163]
	s_mov_b32 m0, s30
	s_nop 0
	global_load_lds_dwordx4 v[182:183], off
	s_mov_b32 m0, s31
	s_nop 0
	global_load_lds_dwordx4 v[184:185], off
	s_waitcnt vmcnt(8)
	s_waitcnt lgkmcnt(0)
	s_barrier
	s_setprio 1
	s_nop 3
	s_waitcnt lgkmcnt(0)
	v_mfma_scale_f32_16x16x128_f8f6f4 v[94:97], v[26:33], v[194:201], 0, v191, v192 op_sel_hi:[0,0,0]
	v_mfma_scale_f32_16x16x128_f8f6f4 v[90:93], v[18:25], v[194:201], 0, v191, v192 op_sel_hi:[0,0,0]
	v_mfma_scale_f32_16x16x128_f8f6f4 v[78:81], v[26:33], v[202:209], 0, v191, v192 op_sel_hi:[0,0,0]
	v_mfma_scale_f32_16x16x128_f8f6f4 v[74:77], v[18:25], v[202:209], 0, v191, v192 op_sel_hi:[0,0,0]
	v_mfma_scale_f32_16x16x128_f8f6f4 v[62:65], v[26:33], v[210:217], 0, v191, v192 op_sel_hi:[0,0,0]
	v_mfma_scale_f32_16x16x128_f8f6f4 v[58:61], v[18:25], v[210:217], 0, v191, v192 op_sel_hi:[0,0,0]
	v_mfma_scale_f32_16x16x128_f8f6f4 v[46:49], v[26:33], v[218:225], 0, v191, v192 op_sel_hi:[0,0,0]
	v_mfma_scale_f32_16x16x128_f8f6f4 v[42:45], v[18:25], v[218:225], 0, v191, v192 op_sel_hi:[0,0,0]
	s_setprio 0
	s_setprio 1
	s_nop 3
	v_mfma_scale_f32_16x16x128_f8f6f4 v[86:89], v[10:17], v[194:201], 0, v191, v192 op_sel_hi:[0,0,0]
	v_mfma_scale_f32_16x16x128_f8f6f4 v[82:85], v[2:9], v[194:201], 0, v191, v192 op_sel_hi:[0,0,0]
	v_mfma_scale_f32_16x16x128_f8f6f4 v[70:73], v[10:17], v[202:209], 0, v191, v192 op_sel_hi:[0,0,0]
	v_mfma_scale_f32_16x16x128_f8f6f4 v[66:69], v[2:9], v[202:209], 0, v191, v192 op_sel_hi:[0,0,0]
	v_mfma_scale_f32_16x16x128_f8f6f4 v[54:57], v[10:17], v[210:217], 0, v191, v192 op_sel_hi:[0,0,0]
	v_mfma_scale_f32_16x16x128_f8f6f4 v[50:53], v[2:9], v[210:217], 0, v191, v192 op_sel_hi:[0,0,0]
	v_mfma_scale_f32_16x16x128_f8f6f4 v[38:41], v[10:17], v[218:225], 0, v191, v192 op_sel_hi:[0,0,0]
	v_mfma_scale_f32_16x16x128_f8f6f4 v[34:37], v[2:9], v[218:225], 0, v191, v192 op_sel_hi:[0,0,0]
	s_setprio 0
	s_barrier
; #define PG8_STAGE(bufoff, gbase, voff) do { _Pragma("unroll") for (int _i = 0; _i < 2; ++_i) \
;         __builtin_amdgcn_global_load_lds((const unsigned*)((const char*)(gbase) + (voff)[_i]), (PG8_LAS unsigned*)(lds + (bufoff) + ldsw + _i * 8192), 16, 0, 0); } while (0)
; #define PG8_STAGE_A(bufoff, gbase, h, nx) do { if constexpr (Sched::GATHER) { const unsigned vv_[2] = {(nx) ? vAn[h][0] : vA[h][0], (nx) ? vAn[h][1] : vA[h][1]}; PG8_STAGE(bufoff, gbase, vv_); } \
;         else { PG8_STAGE(bufoff, (gbase) + (h) * hstep, voffA); } } while (0)
; #define PG8_LDA(dst, b, h) do { _Pragma("unroll") for (int m = 0; m < 4; ++m) _Pragma("unroll") for (int k = 0; k < 2; ++k) dst[m][k] = *(const PG8_LAS bf16x8*)(lds + PG8_SA(b, h) + aoff + m * 2048 + k * 1024); } while (0)
; #define PG8_LDB(dst, b, h) do { _Pragma("unroll") for (int n = 0; n < 2; ++n) _Pragma("unroll") for (int k = 0; k < 2; ++k) dst[n][k] = *(const PG8_LAS bf16x8*)(lds + PG8_SB(b, h) + boff + n * 2048 + k * 1024); } while (0)
; #define PG8_WAIT_V(n) asm volatile("s_waitcnt vmcnt(" #n ")" ::: "memory")
; #define PG8_WAIT_L(n) asm volatile("s_waitcnt lgkmcnt(" #n ")" ::: "memory")
; #define PG8_BAR __builtin_amdgcn_s_barrier()
; #define PG8_SCHED __builtin_amdgcn_sched_barrier(0)
;     ...
;             PG8_LDB(B0, 1, 0); PG8_LDB(B1, 1, 1); PG8_SCHED; PG8_LDA(At, 1, 0); PG8_STAGE_A(PG8_SA(0, 1), a2, 1, last);
;             PG8_WAIT_V(8); PG8_WAIT_L(0); PG8_BAR; PG8_MMA(0, 0, At, B0); PG8_MMA(0, 1, At, B1); PG8_BAR; PG8_SCHED;
;             PG8_LDA(At, 1, 1); PG8_STAGE(PG8_SB(1, 0), b3, voffB); PG8_STAGE(PG8_SB(1, 1), b3 + hstepB, voffB); PG8_STAGE_A(PG8_SA(1, 0), a3, 0, last);
;             PG8_WAIT_V(8); PG8_WAIT_L(0); PG8_BAR; PG8_MMA(1, 0, At, B0); PG8_MMA(1, 1, At, B1); PG8_BAR; PG8_SCHED;
	s_add_i32 s44, 0, 0x18000
	s_add_i32 s45, 0, 0x1c000
	v_add_u32_e32 v14, s44, v186
	v_add_u32_e32 v30, s45, v186
	ds_read_b128 v[2:5], v14
	ds_read_b128 v[6:9], v14 offset:1024
	ds_read_b128 v[10:13], v14 offset:2048
	ds_read_b128 v[14:17], v14 offset:3072
	ds_read_b128 v[18:21], v30
	ds_read_b128 v[22:25], v30 offset:1024
	ds_read_b128 v[26:29], v30 offset:2048
	ds_read_b128 v[30:33], v30 offset:3072
	s_add_u32 s26, s26, 0x20000
	s_addc_u32 s27, s27, 0
	s_mov_b32 m0, s34
	v_lshl_add_u64 v[226:227], s[26:27], 0, v[162:163]
	ds_read_b128 v[194:197], v190 offset:32768
	ds_read_b128 v[198:201], v190 offset:33792
	ds_read_b128 v[202:205], v190 offset:34816
	ds_read_b128 v[206:209], v190 offset:35840
	ds_read_b128 v[210:213], v190 offset:36864
	ds_read_b128 v[214:217], v190 offset:37888
	ds_read_b128 v[218:221], v190 offset:38912
	ds_read_b128 v[222:225], v190 offset:39936
	global_load_lds_dwordx4 v[226:227], off
	v_lshl_add_u64 v[226:227], s[26:27], 0, v[166:167]
	s_mov_b32 m0, s35
	s_nop 0
	global_load_lds_dwordx4 v[226:227], off
	s_waitcnt vmcnt(8)
	s_waitcnt lgkmcnt(0)
	s_barrier
	s_setprio 1
	s_nop 3
	s_waitcnt lgkmcnt(0)
	v_mfma_scale_f32_16x16x128_f8f6f4 v[158:161], v[2:9], v[194:201], v[158:161], v191, v192 op_sel_hi:[0,0,0]
	v_mfma_scale_f32_16x16x128_f8f6f4 v[154:157], v[10:17], v[194:201], v[154:157], v191, v192 op_sel_hi:[0,0,0]
	v_mfma_scale_f32_16x16x128_f8f6f4 v[142:145], v[2:9], v[202:209], v[142:145], v191, v192 op_sel_hi:[0,0,0]
	v_mfma_scale_f32_16x16x128_f8f6f4 v[138:141], v[10:17], v[202:209], v[138:141], v191, v192 op_sel_hi:[0,0,0]
	v_mfma_scale_f32_16x16x128_f8f6f4 v[126:129], v[2:9], v[210:217], v[126:129], v191, v192 op_sel_hi:[0,0,0]
	v_mfma_scale_f32_16x16x128_f8f6f4 v[122:125], v[10:17], v[210:217], v[122:125], v191, v192 op_sel_hi:[0,0,0]
	v_mfma_scale_f32_16x16x128_f8f6f4 v[110:113], v[2:9], v[218:225], v[110:113], v191, v192 op_sel_hi:[0,0,0]
	v_mfma_scale_f32_16x16x128_f8f6f4 v[106:109], v[10:17], v[218:225], v[106:109], v191, v192 op_sel_hi:[0,0,0]
	s_setprio 0
	s_setprio 1
	s_nop 3
	v_mfma_scale_f32_16x16x128_f8f6f4 v[150:153], v[18:25], v[194:201], v[150:153], v191, v192 op_sel_hi:[0,0,0]
	v_mfma_scale_f32_16x16x128_f8f6f4 v[146:149], v[26:33], v[194:201], v[146:149], v191, v192 op_sel_hi:[0,0,0]
	v_mfma_scale_f32_16x16x128_f8f6f4 v[134:137], v[18:25], v[202:209], v[134:137], v191, v192 op_sel_hi:[0,0,0]
	v_mfma_scale_f32_16x16x128_f8f6f4 v[130:133], v[26:33], v[202:209], v[130:133], v191, v192 op_sel_hi:[0,0,0]
	v_mfma_scale_f32_16x16x128_f8f6f4 v[118:121], v[18:25], v[210:217], v[118:121], v191, v192 op_sel_hi:[0,0,0]
	v_mfma_scale_f32_16x16x128_f8f6f4 v[114:117], v[26:33], v[210:217], v[114:117], v191, v192 op_sel_hi:[0,0,0]
	v_mfma_scale_f32_16x16x128_f8f6f4 v[102:105], v[18:25], v[218:225], v[102:105], v191, v192 op_sel_hi:[0,0,0]
	v_mfma_scale_f32_16x16x128_f8f6f4 v[98:101], v[26:33], v[218:225], v[98:101], v191, v192 op_sel_hi:[0,0,0]
	s_setprio 0
	s_barrier
	s_add_i32 s26, s44, s28
	v_lshl_add_u64 v[178:179], v[178:179], 0, s[8:9]
	s_mov_b32 m0, s26
	ds_read_b128 v[194:197], v190 offset:49152
	ds_read_b128 v[198:201], v190 offset:50176
	ds_read_b128 v[202:205], v190 offset:51200
	ds_read_b128 v[206:209], v190 offset:52224
	ds_read_b128 v[210:213], v190 offset:53248
	ds_read_b128 v[214:217], v190 offset:54272
	ds_read_b128 v[218:221], v190 offset:55296
	ds_read_b128 v[222:225], v190 offset:56320
	global_load_lds_dwordx4 v[178:179], off
	s_add_i32 m0, s26, 0x2000
	s_add_u32 s24, s24, 0x2080
	v_lshl_add_u64 v[178:179], v[180:181], 0, s[8:9]
	s_addc_u32 s25, s25, 0
	s_add_i32 s26, s45, s28
	global_load_lds_dwordx4 v[178:179], off
	v_lshl_add_u64 v[178:179], s[24:25], 0, v[164:165]
	s_mov_b32 m0, s26
	s_nop 0
	global_load_lds_dwordx4 v[178:179], off
	v_lshl_add_u64 v[178:179], s[24:25], 0, v[168:169]
	s_add_i32 m0, s26, 0x2000
	s_nop 0
	global_load_lds_dwordx4 v[178:179], off
	v_lshl_add_u64 v[178:179], v[182:183], 0, s[8:9]
	s_mov_b32 m0, s38
	s_nop 0
	global_load_lds_dwordx4 v[178:179], off
	v_lshl_add_u64 v[178:179], v[184:185], 0, s[8:9]
	s_mov_b32 m0, s39
	s_nop 0
	global_load_lds_dwordx4 v[178:179], off
	s_waitcnt vmcnt(8)
	s_waitcnt lgkmcnt(0)
	s_barrier
	s_setprio 1
	s_nop 3
	s_waitcnt lgkmcnt(0)
	v_mfma_scale_f32_16x16x128_f8f6f4 v[94:97], v[2:9], v[194:201], v[94:97], v191, v192 op_sel_hi:[0,0,0]
	v_mfma_scale_f32_16x16x128_f8f6f4 v[90:93], v[10:17], v[194:201], v[90:93], v191, v192 op_sel_hi:[0,0,0]
	v_mfma_scale_f32_16x16x128_f8f6f4 v[78:81], v[2:9], v[202:209], v[78:81], v191, v192 op_sel_hi:[0,0,0]
	v_mfma_scale_f32_16x16x128_f8f6f4 v[74:77], v[10:17], v[202:209], v[74:77], v191, v192 op_sel_hi:[0,0,0]
	v_mfma_scale_f32_16x16x128_f8f6f4 v[62:65], v[2:9], v[210:217], v[62:65], v191, v192 op_sel_hi:[0,0,0]
	v_mfma_scale_f32_16x16x128_f8f6f4 v[58:61], v[10:17], v[210:217], v[58:61], v191, v192 op_sel_hi:[0,0,0]
	v_mfma_scale_f32_16x16x128_f8f6f4 v[46:49], v[2:9], v[218:225], v[46:49], v191, v192 op_sel_hi:[0,0,0]
	v_mfma_scale_f32_16x16x128_f8f6f4 v[42:45], v[10:17], v[218:225], v[42:45], v191, v192 op_sel_hi:[0,0,0]
	s_setprio 0
	s_setprio 1
	s_nop 3
	v_mfma_scale_f32_16x16x128_f8f6f4 v[86:89], v[18:25], v[194:201], v[86:89], v191, v192 op_sel_hi:[0,0,0]
	v_mfma_scale_f32_16x16x128_f8f6f4 v[82:85], v[26:33], v[194:201], v[82:85], v191, v192 op_sel_hi:[0,0,0]
	v_mfma_scale_f32_16x16x128_f8f6f4 v[70:73], v[18:25], v[202:209], v[70:73], v191, v192 op_sel_hi:[0,0,0]
	v_mfma_scale_f32_16x16x128_f8f6f4 v[66:69], v[26:33], v[202:209], v[66:69], v191, v192 op_sel_hi:[0,0,0]
	v_mfma_scale_f32_16x16x128_f8f6f4 v[54:57], v[18:25], v[210:217], v[54:57], v191, v192 op_sel_hi:[0,0,0]
	v_mfma_scale_f32_16x16x128_f8f6f4 v[50:53], v[26:33], v[210:217], v[50:53], v191, v192 op_sel_hi:[0,0,0]
	v_mfma_scale_f32_16x16x128_f8f6f4 v[38:41], v[18:25], v[218:225], v[38:41], v191, v192 op_sel_hi:[0,0,0]
	v_mfma_scale_f32_16x16x128_f8f6f4 v[34:37], v[26:33], v[218:225], v[34:37], v191, v192 op_sel_hi:[0,0,0]
	s_setprio 0
	s_barrier
	s_add_i32 s43, s43, 2
	s_add_u32 s22, s22, 0x100
	s_addc_u32 s23, s23, 0
	s_add_u32 s33, s33, 0x100
	s_addc_u32 s42, s42, 0
; #define PG8_STAGE(bufoff, gbase, voff) do { _Pragma("unroll") for (int _i = 0; _i < 2; ++_i) \
;         __builtin_amdgcn_global_load_lds((const unsigned*)((const char*)(gbase) + (voff)[_i]), (PG8_LAS unsigned*)(lds + (bufoff) + ldsw + _i * 8192), 16, 0, 0); } while (0)
; #define PG8_STAGE_A(bufoff, gbase, h, nx) do { if constexpr (Sched::GATHER) { const unsigned vv_[2] = {(nx) ? vAn[h][0] : vA[h][0], (nx) ? vAn[h][1] : vA[h][1]}; PG8_STAGE(bufoff, gbase, vv_); } \
;         else { PG8_STAGE(bufoff, (gbase) + (h) * hstep, voffA); } } while (0)
; #define PG8_LDA(dst, b, h) do { _Pragma("unroll") for (int m = 0; m < 4; ++m) _Pragma("unroll") for (int k = 0; k < 2; ++k) dst[m][k] = *(const PG8_LAS bf16x8*)(lds + PG8_SA(b, h) + aoff + m * 2048 + k * 1024); } while (0)
; #define PG8_LDB(dst, b, h) do { _Pragma("unroll") for (int n = 0; n < 2; ++n) _Pragma("unroll") for (int k = 0; k < 2; ++k) dst[n][k] = *(const PG8_LAS bf16x8*)(lds + PG8_SB(b, h) + boff + n * 2048 + k * 1024); } while (0)
; #define PG8_WAIT_V(n) asm volatile("s_waitcnt vmcnt(" #n ")" ::: "memory")
; #define PG8_WAIT_L(n) asm volatile("s_waitcnt lgkmcnt(" #n ")" ::: "memory")
; #define PG8_BAR __builtin_amdgcn_s_barrier()
; #define PG8_SCHED __builtin_amdgcn_sched_barrier(0)
;     ...
;         for (int t = 0; t < nt; t += 2) {
;             const bool last = (t == nt - 2);
;             const char* a1 = cA + (size_t)(t + 1) * kstep;
;             const char* a2 = last ? nA : cA + (size_t)(t + 2) * kstep; const char* b2 = last ? nB : cB + (size_t)(t + 2) * kstep;
;             const char* a3 = a2 + kstep; const char* b3 = b2 + kstep;
;             if (last && has_next) S.a_ready(nxt);
;             if constexpr (SP2) {
;             PG8_LDB(B0, 0, 0); PG8_LDB(B1, 0, 1); PG8_SCHED; PG8_LDA(At, 0, 0); PG8_STAGE_A(PG8_SA(1, 1), a1, 1, false);
;             PG8_WAIT_V(8); PG8_WAIT_L(0); PG8_BAR; PG8_MMA(0, 0, At, B0); PG8_MMA(0, 1, At, B1); PG8_BAR; PG8_SCHED;
;             PG8_LDA(At, 0, 1); PG8_STAGE(PG8_SB(0, 0), b2, voffB); PG8_STAGE(PG8_SB(0, 1), b2 + hstepB, voffB); PG8_STAGE_A(PG8_SA(0, 0), a2, 0, last);
;             PG8_WAIT_V(8); PG8_WAIT_L(0); PG8_BAR; PG8_MMA(1, 0, At, B0); PG8_MMA(1, 1, At, B1); PG8_BAR; PG8_SCHED;
.LBB0_474:
	ds_read_b128 v[26:29], v188
	ds_read_b128 v[30:33], v188 offset:1024
	ds_read_b128 v[18:21], v188 offset:2048
	ds_read_b128 v[22:25], v188 offset:3072
	ds_read_b128 v[10:13], v189
	ds_read_b128 v[14:17], v189 offset:1024
	ds_read_b128 v[2:5], v189 offset:2048
	ds_read_b128 v[6:9], v189 offset:3072
	s_add_u32 s24, s22, 0xfffe0080
	s_addc_u32 s25, s23, -1
	s_cmp_eq_u32 s43, 4
	s_cselect_b32 s27, s1, s25
	s_cselect_b32 s26, s15, s24
	s_cselect_b32 s25, s13, s42
	s_cselect_b32 s24, s21, s33
	v_lshl_add_u64 v[218:219], s[22:23], 0, v[170:171]
	s_add_i32 m0, s30, 0xc000
	ds_read_b128 v[178:181], v190
	ds_read_b128 v[182:185], v190 offset:1024
	ds_read_b128 v[194:197], v190 offset:2048
	ds_read_b128 v[198:201], v190 offset:3072
	ds_read_b128 v[202:205], v190 offset:4096
	ds_read_b128 v[206:209], v190 offset:5120
	ds_read_b128 v[210:213], v190 offset:6144
	ds_read_b128 v[214:217], v190 offset:7168
	global_load_lds_dwordx4 v[218:219], off
	v_lshl_add_u64 v[218:219], s[22:23], 0, v[172:173]
	s_add_i32 m0, s30, 0xe000
	s_nop 0
	global_load_lds_dwordx4 v[218:219], off
	s_waitcnt vmcnt(8)
	s_waitcnt lgkmcnt(0)
	s_barrier
	s_setprio 1
	s_nop 3
	s_waitcnt lgkmcnt(0)
	v_mfma_scale_f32_16x16x128_f8f6f4 v[158:161], v[26:33], v[178:185], v[158:161], v191, v192 op_sel_hi:[0,0,0]
	v_mfma_scale_f32_16x16x128_f8f6f4 v[154:157], v[18:25], v[178:185], v[154:157], v191, v192 op_sel_hi:[0,0,0]
	v_mfma_scale_f32_16x16x128_f8f6f4 v[142:145], v[26:33], v[194:201], v[142:145], v191, v192 op_sel_hi:[0,0,0]
	v_mfma_scale_f32_16x16x128_f8f6f4 v[138:141], v[18:25], v[194:201], v[138:141], v191, v192 op_sel_hi:[0,0,0]
	v_mfma_scale_f32_16x16x128_f8f6f4 v[126:129], v[26:33], v[202:209], v[126:129], v191, v192 op_sel_hi:[0,0,0]
	v_mfma_scale_f32_16x16x128_f8f6f4 v[122:125], v[18:25], v[202:209], v[122:125], v191, v192 op_sel_hi:[0,0,0]
	v_mfma_scale_f32_16x16x128_f8f6f4 v[110:113], v[26:33], v[210:217], v[110:113], v191, v192 op_sel_hi:[0,0,0]
	v_mfma_scale_f32_16x16x128_f8f6f4 v[106:109], v[18:25], v[210:217], v[106:109], v191, v192 op_sel_hi:[0,0,0]
	s_setprio 0
	s_setprio 1
	s_nop 3
	v_mfma_scale_f32_16x16x128_f8f6f4 v[150:153], v[10:17], v[178:185], v[150:153], v191, v192 op_sel_hi:[0,0,0]
	v_mfma_scale_f32_16x16x128_f8f6f4 v[146:149], v[2:9], v[178:185], v[146:149], v191, v192 op_sel_hi:[0,0,0]
	v_mfma_scale_f32_16x16x128_f8f6f4 v[134:137], v[10:17], v[194:201], v[134:137], v191, v192 op_sel_hi:[0,0,0]
	v_mfma_scale_f32_16x16x128_f8f6f4 v[130:133], v[2:9], v[194:201], v[130:133], v191, v192 op_sel_hi:[0,0,0]
	v_mfma_scale_f32_16x16x128_f8f6f4 v[118:121], v[10:17], v[202:209], v[118:121], v191, v192 op_sel_hi:[0,0,0]
	v_mfma_scale_f32_16x16x128_f8f6f4 v[114:117], v[2:9], v[202:209], v[114:117], v191, v192 op_sel_hi:[0,0,0]
	v_mfma_scale_f32_16x16x128_f8f6f4 v[102:105], v[10:17], v[210:217], v[102:105], v191, v192 op_sel_hi:[0,0,0]
	v_mfma_scale_f32_16x16x128_f8f6f4 v[98:101], v[2:9], v[210:217], v[98:101], v191, v192 op_sel_hi:[0,0,0]
	s_setprio 0
	s_barrier
	s_add_i32 s44, s40, s28
	v_lshl_add_u64 v[178:179], s[24:25], 0, v[164:165]
	s_mov_b32 m0, s44
	ds_read_b128 v[194:197], v190 offset:16384
	ds_read_b128 v[198:201], v190 offset:17408
	ds_read_b128 v[202:205], v190 offset:18432
	ds_read_b128 v[206:209], v190 offset:19456
	ds_read_b128 v[210:213], v190 offset:20480
	ds_read_b128 v[214:217], v190 offset:21504
	ds_read_b128 v[218:221], v190 offset:22528
	ds_read_b128 v[222:225], v190 offset:23552
	global_load_lds_dwordx4 v[178:179], off
	s_add_i32 m0, s44, 0x2000
	s_add_u32 s44, s24, 0x2000
	v_lshl_add_u64 v[180:181], s[24:25], 0, v[168:169]
	s_addc_u32 s45, s25, 0
	s_add_i32 s46, s41, s28
	global_load_lds_dwordx4 v[180:181], off
	v_lshl_add_u64 v[182:183], s[44:45], 0, v[164:165]
	s_mov_b32 m0, s46
	v_lshl_add_u64 v[184:185], s[26:27], 0, v[166:167]
	global_load_lds_dwordx4 v[182:183], off
	v_lshl_add_u64 v[182:183], s[44:45], 0, v[168:169]
	s_add_i32 m0, s46, 0x2000
	s_nop 0
	global_load_lds_dwordx4 v[182:183], off
	v_lshl_add_u64 v[182:183], s[26:27], 0, v[162:163]
	s_mov_b32 m0, s30
	s_nop 0
	global_load_lds_dwordx4 v[182:183], off
	s_mov_b32 m0, s31
	s_nop 0
	global_load_lds_dwordx4 v[184:185], off
	s_waitcnt vmcnt(8)
	s_waitcnt lgkmcnt(0)
	s_barrier
	s_setprio 1
	s_nop 3
	s_waitcnt lgkmcnt(0)
	v_mfma_scale_f32_16x16x128_f8f6f4 v[94:97], v[26:33], v[194:201], v[94:97], v191, v192 op_sel_hi:[0,0,0]
	v_mfma_scale_f32_16x16x128_f8f6f4 v[90:93], v[18:25], v[194:201], v[90:93], v191, v192 op_sel_hi:[0,0,0]
	v_mfma_scale_f32_16x16x128_f8f6f4 v[78:81], v[26:33], v[202:209], v[78:81], v191, v192 op_sel_hi:[0,0,0]
	v_mfma_scale_f32_16x16x128_f8f6f4 v[74:77], v[18:25], v[202:209], v[74:77], v191, v192 op_sel_hi:[0,0,0]
	v_mfma_scale_f32_16x16x128_f8f6f4 v[62:65], v[26:33], v[210:217], v[62:65], v191, v192 op_sel_hi:[0,0,0]
	v_mfma_scale_f32_16x16x128_f8f6f4 v[58:61], v[18:25], v[210:217], v[58:61], v191, v192 op_sel_hi:[0,0,0]
	v_mfma_scale_f32_16x16x128_f8f6f4 v[46:49], v[26:33], v[218:225], v[46:49], v191, v192 op_sel_hi:[0,0,0]
	v_mfma_scale_f32_16x16x128_f8f6f4 v[42:45], v[18:25], v[218:225], v[42:45], v191, v192 op_sel_hi:[0,0,0]
	s_setprio 0
	s_setprio 1
	s_nop 3
	v_mfma_scale_f32_16x16x128_f8f6f4 v[86:89], v[10:17], v[194:201], v[86:89], v191, v192 op_sel_hi:[0,0,0]
	v_mfma_scale_f32_16x16x128_f8f6f4 v[82:85], v[2:9], v[194:201], v[82:85], v191, v192 op_sel_hi:[0,0,0]
	v_mfma_scale_f32_16x16x128_f8f6f4 v[70:73], v[10:17], v[202:209], v[70:73], v191, v192 op_sel_hi:[0,0,0]
	v_mfma_scale_f32_16x16x128_f8f6f4 v[66:69], v[2:9], v[202:209], v[66:69], v191, v192 op_sel_hi:[0,0,0]
	v_mfma_scale_f32_16x16x128_f8f6f4 v[54:57], v[10:17], v[210:217], v[54:57], v191, v192 op_sel_hi:[0,0,0]
	v_mfma_scale_f32_16x16x128_f8f6f4 v[50:53], v[2:9], v[210:217], v[50:53], v191, v192 op_sel_hi:[0,0,0]
	v_mfma_scale_f32_16x16x128_f8f6f4 v[38:41], v[10:17], v[218:225], v[38:41], v191, v192 op_sel_hi:[0,0,0]
	v_mfma_scale_f32_16x16x128_f8f6f4 v[34:37], v[2:9], v[218:225], v[34:37], v191, v192 op_sel_hi:[0,0,0]
	s_setprio 0
	s_barrier
; #define PG8_STAGE(bufoff, gbase, voff) do { _Pragma("unroll") for (int _i = 0; _i < 2; ++_i) \
;         __builtin_amdgcn_global_load_lds((const unsigned*)((const char*)(gbase) + (voff)[_i]), (PG8_LAS unsigned*)(lds + (bufoff) + ldsw + _i * 8192), 16, 0, 0); } while (0)
; #define PG8_WAIT_V(n) asm volatile("s_waitcnt vmcnt(" #n ")" ::: "memory")
; #define PG8_WAIT_L(n) asm volatile("s_waitcnt lgkmcnt(" #n ")" ::: "memory")
;     ...
;             PG8_LDB(B0, 1, 0); PG8_LDB(B1, 1, 1); PG8_SCHED; PG8_LDA(At, 1, 0); PG8_STAGE_A(PG8_SA(0, 1), a2, 1, last);
;             PG8_WAIT_V(8); PG8_WAIT_L(0); PG8_BAR; PG8_MMA(0, 0, At, B0); PG8_MMA(0, 1, At, B1); PG8_BAR; PG8_SCHED;
;             PG8_LDA(At, 1, 1); PG8_STAGE(PG8_SB(1, 0), b3, voffB); PG8_STAGE(PG8_SB(1, 1), b3 + hstepB, voffB); PG8_STAGE_A(PG8_SA(1, 0), a3, 0, last);
;             PG8_WAIT_V(8); PG8_WAIT_L(0); PG8_BAR; PG8_MMA(1, 0, At, B0); PG8_MMA(1, 1, At, B1); PG8_BAR; PG8_SCHED;
;             } else {
;             PG8_LDB(B0, 0, 0); PG8_SCHED; PG8_LDA(At, 0, 0); PG8_STAGE(PG8_SA(1, 1), a1 + hstep, voffA);
;             PG8_WAIT_L(8); PG8_BAR; PG8_WAIT_L(0); PG8_MMA(0, 0, At, B0); PG8_BAR; PG8_SCHED;
;             PG8_LDB(B1, 0, 1); PG8_STAGE(PG8_SB(0, 0), b2, voffB);
;             PG8_BAR; PG8_WAIT_L(0); PG8_MMA(0, 1, At, B1); PG8_BAR;
;             PG8_LDA(At, 0, 1); PG8_STAGE(PG8_SA(0, 0), a2, voffA);
;             PG8_BAR; PG8_WAIT_L(0); PG8_MMA(1, 0, At, B0); PG8_BAR; PG8_SCHED;
;             PG8_STAGE(PG8_SB(0, 1), b2 + hstepB, voffB);
;             PG8_WAIT_V(6); PG8_BAR; PG8_MMA(1, 1, At, B1); PG8_BAR;
;             PG8_LDB(B0, 1, 0); PG8_SCHED; PG8_LDA(At, 1, 0); PG8_STAGE(PG8_SA(0, 1), a2 + hstep, voffA);
;             PG8_WAIT_L(8); PG8_BAR; PG8_WAIT_L(0); PG8_MMA(0, 0, At, B0); PG8_BAR; PG8_SCHED;
;             PG8_LDB(B1, 1, 1); PG8_STAGE(PG8_SB(1, 0), b3, voffB);
;             PG8_BAR; PG8_WAIT_L(0); PG8_MMA(0, 1, At, B1); PG8_BAR;
;             PG8_LDA(At, 1, 1); PG8_STAGE(PG8_SA(1, 0), a3, voffA);
;             PG8_BAR; PG8_WAIT_L(0); PG8_MMA(1, 0, At, B0); PG8_BAR; PG8_SCHED;
;             PG8_STAGE(PG8_SB(1, 1), b3 + hstepB, voffB);
;             PG8_WAIT_V(6); PG8_BAR; PG8_MMA(1, 1, At, B1); PG8_BAR;
;             }
;         }
;         if constexpr (F8) asm volatile("s_nop 15\n\ts_nop 15\n\ts_nop 15" ::: "memory");
;         if constexpr (ALIGN_EPI) { if (wr == 0) PG8_BAR; }
	s_add_i32 s44, 0, 0x18000
	s_add_i32 s45, 0, 0x1c000
	v_add_u32_e32 v14, s44, v186
	v_add_u32_e32 v30, s45, v186
	ds_read_b128 v[2:5], v14
	ds_read_b128 v[6:9], v14 offset:1024
	ds_read_b128 v[10:13], v14 offset:2048
	ds_read_b128 v[14:17], v14 offset:3072
	ds_read_b128 v[18:21], v30
	ds_read_b128 v[22:25], v30 offset:1024
	ds_read_b128 v[26:29], v30 offset:2048
	ds_read_b128 v[30:33], v30 offset:3072
	s_add_u32 s26, s26, 0x20000
	s_addc_u32 s27, s27, 0
	s_mov_b32 m0, s34
	v_lshl_add_u64 v[226:227], s[26:27], 0, v[162:163]
	ds_read_b128 v[194:197], v190 offset:32768
	ds_read_b128 v[198:201], v190 offset:33792
	ds_read_b128 v[202:205], v190 offset:34816
	ds_read_b128 v[206:209], v190 offset:35840
	ds_read_b128 v[210:213], v190 offset:36864
	ds_read_b128 v[214:217], v190 offset:37888
	ds_read_b128 v[218:221], v190 offset:38912
	ds_read_b128 v[222:225], v190 offset:39936
	global_load_lds_dwordx4 v[226:227], off
	v_lshl_add_u64 v[226:227], s[26:27], 0, v[166:167]
	s_mov_b32 m0, s35
	s_nop 0
	global_load_lds_dwordx4 v[226:227], off
	s_waitcnt vmcnt(8)
	s_waitcnt lgkmcnt(0)
	s_barrier
	s_setprio 1
	s_nop 3
	s_waitcnt lgkmcnt(0)
	v_mfma_scale_f32_16x16x128_f8f6f4 v[158:161], v[2:9], v[194:201], v[158:161], v191, v192 op_sel_hi:[0,0,0]
	v_mfma_scale_f32_16x16x128_f8f6f4 v[154:157], v[10:17], v[194:201], v[154:157], v191, v192 op_sel_hi:[0,0,0]
	v_mfma_scale_f32_16x16x128_f8f6f4 v[142:145], v[2:9], v[202:209], v[142:145], v191, v192 op_sel_hi:[0,0,0]
	v_mfma_scale_f32_16x16x128_f8f6f4 v[138:141], v[10:17], v[202:209], v[138:141], v191, v192 op_sel_hi:[0,0,0]
	v_mfma_scale_f32_16x16x128_f8f6f4 v[126:129], v[2:9], v[210:217], v[126:129], v191, v192 op_sel_hi:[0,0,0]
	v_mfma_scale_f32_16x16x128_f8f6f4 v[122:125], v[10:17], v[210:217], v[122:125], v191, v192 op_sel_hi:[0,0,0]
	v_mfma_scale_f32_16x16x128_f8f6f4 v[110:113], v[2:9], v[218:225], v[110:113], v191, v192 op_sel_hi:[0,0,0]
	v_mfma_scale_f32_16x16x128_f8f6f4 v[106:109], v[10:17], v[218:225], v[106:109], v191, v192 op_sel_hi:[0,0,0]
	s_setprio 0
	s_setprio 1
	s_nop 3
	v_mfma_scale_f32_16x16x128_f8f6f4 v[150:153], v[18:25], v[194:201], v[150:153], v191, v192 op_sel_hi:[0,0,0]
	v_mfma_scale_f32_16x16x128_f8f6f4 v[146:149], v[26:33], v[194:201], v[146:149], v191, v192 op_sel_hi:[0,0,0]
	v_mfma_scale_f32_16x16x128_f8f6f4 v[134:137], v[18:25], v[202:209], v[134:137], v191, v192 op_sel_hi:[0,0,0]
	v_mfma_scale_f32_16x16x128_f8f6f4 v[130:133], v[26:33], v[202:209], v[130:133], v191, v192 op_sel_hi:[0,0,0]
	v_mfma_scale_f32_16x16x128_f8f6f4 v[118:121], v[18:25], v[210:217], v[118:121], v191, v192 op_sel_hi:[0,0,0]
	v_mfma_scale_f32_16x16x128_f8f6f4 v[114:117], v[26:33], v[210:217], v[114:117], v191, v192 op_sel_hi:[0,0,0]
	v_mfma_scale_f32_16x16x128_f8f6f4 v[102:105], v[18:25], v[218:225], v[102:105], v191, v192 op_sel_hi:[0,0,0]
	v_mfma_scale_f32_16x16x128_f8f6f4 v[98:101], v[26:33], v[218:225], v[98:101], v191, v192 op_sel_hi:[0,0,0]
	s_setprio 0
	s_barrier
	s_add_i32 s26, s44, s28
	v_lshl_add_u64 v[178:179], v[178:179], 0, s[8:9]
	s_mov_b32 m0, s26
	ds_read_b128 v[194:197], v190 offset:49152
	ds_read_b128 v[198:201], v190 offset:50176
	ds_read_b128 v[202:205], v190 offset:51200
	ds_read_b128 v[206:209], v190 offset:52224
	ds_read_b128 v[210:213], v190 offset:53248
	ds_read_b128 v[214:217], v190 offset:54272
	ds_read_b128 v[218:221], v190 offset:55296
	ds_read_b128 v[222:225], v190 offset:56320
	global_load_lds_dwordx4 v[178:179], off
	s_add_i32 m0, s26, 0x2000
	s_add_u32 s24, s24, 0x2080
	v_lshl_add_u64 v[178:179], v[180:181], 0, s[8:9]
	s_addc_u32 s25, s25, 0
	s_add_i32 s26, s45, s28
	global_load_lds_dwordx4 v[178:179], off
	v_lshl_add_u64 v[178:179], s[24:25], 0, v[164:165]
	s_mov_b32 m0, s26
	s_nop 0
	global_load_lds_dwordx4 v[178:179], off
	v_lshl_add_u64 v[178:179], s[24:25], 0, v[168:169]
	s_add_i32 m0, s26, 0x2000
	s_nop 0
	global_load_lds_dwordx4 v[178:179], off
	v_lshl_add_u64 v[178:179], v[182:183], 0, s[8:9]
	s_mov_b32 m0, s38
	s_nop 0
	global_load_lds_dwordx4 v[178:179], off
	v_lshl_add_u64 v[178:179], v[184:185], 0, s[8:9]
	s_mov_b32 m0, s39
	s_nop 0
	global_load_lds_dwordx4 v[178:179], off
	s_waitcnt vmcnt(8)
	s_waitcnt lgkmcnt(0)
	s_barrier
	s_setprio 1
	s_nop 3
	s_waitcnt lgkmcnt(0)
	v_mfma_scale_f32_16x16x128_f8f6f4 v[94:97], v[2:9], v[194:201], v[94:97], v191, v192 op_sel_hi:[0,0,0]
	v_mfma_scale_f32_16x16x128_f8f6f4 v[90:93], v[10:17], v[194:201], v[90:93], v191, v192 op_sel_hi:[0,0,0]
	v_mfma_scale_f32_16x16x128_f8f6f4 v[78:81], v[2:9], v[202:209], v[78:81], v191, v192 op_sel_hi:[0,0,0]
	v_mfma_scale_f32_16x16x128_f8f6f4 v[74:77], v[10:17], v[202:209], v[74:77], v191, v192 op_sel_hi:[0,0,0]
	v_mfma_scale_f32_16x16x128_f8f6f4 v[62:65], v[2:9], v[210:217], v[62:65], v191, v192 op_sel_hi:[0,0,0]
	v_mfma_scale_f32_16x16x128_f8f6f4 v[58:61], v[10:17], v[210:217], v[58:61], v191, v192 op_sel_hi:[0,0,0]
	v_mfma_scale_f32_16x16x128_f8f6f4 v[46:49], v[2:9], v[218:225], v[46:49], v191, v192 op_sel_hi:[0,0,0]
	v_mfma_scale_f32_16x16x128_f8f6f4 v[42:45], v[10:17], v[218:225], v[42:45], v191, v192 op_sel_hi:[0,0,0]
	s_setprio 0
	s_setprio 1
	s_nop 3
	v_mfma_scale_f32_16x16x128_f8f6f4 v[86:89], v[18:25], v[194:201], v[86:89], v191, v192 op_sel_hi:[0,0,0]
	v_mfma_scale_f32_16x16x128_f8f6f4 v[82:85], v[26:33], v[194:201], v[82:85], v191, v192 op_sel_hi:[0,0,0]
	v_mfma_scale_f32_16x16x128_f8f6f4 v[70:73], v[18:25], v[202:209], v[70:73], v191, v192 op_sel_hi:[0,0,0]
	v_mfma_scale_f32_16x16x128_f8f6f4 v[66:69], v[26:33], v[202:209], v[66:69], v191, v192 op_sel_hi:[0,0,0]
	v_mfma_scale_f32_16x16x128_f8f6f4 v[54:57], v[18:25], v[210:217], v[54:57], v191, v192 op_sel_hi:[0,0,0]
	v_mfma_scale_f32_16x16x128_f8f6f4 v[50:53], v[26:33], v[210:217], v[50:53], v191, v192 op_sel_hi:[0,0,0]
	v_mfma_scale_f32_16x16x128_f8f6f4 v[38:41], v[18:25], v[218:225], v[38:41], v191, v192 op_sel_hi:[0,0,0]
	v_mfma_scale_f32_16x16x128_f8f6f4 v[34:37], v[26:33], v[218:225], v[34:37], v191, v192 op_sel_hi:[0,0,0]
	s_setprio 0
	s_barrier
	s_add_i32 s43, s43, 2
	s_add_u32 s22, s22, 0x100
	s_addc_u32 s23, s23, 0
	s_add_u32 s33, s33, 0x100
	s_addc_u32 s42, s42, 0
	s_cmp_gt_u32 s43, 5
	s_cbranch_scc0 .LBB0_474
	s_and_b64 vcc, exec, s[10:11]
	s_cbranch_vccz .LBB0_477
	s_barrier
; __device__ __forceinline__ unsigned cvt_pk_bf16(float lo, float hi) { unsigned r; asm volatile("v_cvt_pk_bf16_f32 %0, %1, %2" : "=v"(r) : "v"(lo), "v"(hi)); return r; }
;     __device__ __forceinline__ void operator()(const f32x4 (&acc)[2][2][4][2], const Unit& u, int wr, int wc, int fr, int fq) const {
;         const int row0 = u.pm * BM + wr * 64 + fr, col0 = u.pn * BM + wc * 64 + 16 * fq;
; #pragma unroll
;         for (int ai = 0; ai < 2; ++ai)
; #pragma unroll
;             for (int m = 0; m < 4; ++m) { const size_t off = (size_t)(row0 + ai * HALF + m * 16) * ldc + col0;
;                 f32x4 r[4];
;                 if constexpr (RESID_F32) {
; #pragma unroll
;                     for (int p = 0; p < 4; ++p) r[p] = *(const f32x4*)((const float*)resid + off + 4 * p); }
;                 else { const u32x4 w0 = *(const u32x4*)((const bf16_t*)resid + off), w1 = *(const u32x4*)((const bf16_t*)resid + off + 8);
;                     r[0] = (f32x4){__uint_as_float(w0.x << 16), __uint_as_float(w0.x & 0xffff0000u), __uint_as_float(w0.y << 16), __uint_as_float(w0.y & 0xffff0000u)};
;                     r[1] = (f32x4){__uint_as_float(w0.z << 16), __uint_as_float(w0.z & 0xffff0000u), __uint_as_float(w0.w << 16), __uint_as_float(w0.w & 0xffff0000u)};
;                     r[2] = (f32x4){__uint_as_float(w1.x << 16), __uint_as_float(w1.x & 0xffff0000u), __uint_as_float(w1.y << 16), __uint_as_float(w1.y & 0xffff0000u)};
;                     r[3] = (f32x4){__uint_as_float(w1.z << 16), __uint_as_float(w1.z & 0xffff0000u), __uint_as_float(w1.w << 16), __uint_as_float(w1.w & 0xffff0000u)}; }
;                 unsigned o[8];
; #pragma unroll
;                 for (int bj = 0; bj < 2; ++bj)
; #pragma unroll
;                     for (int n = 0; n < 2; ++n) { const f32x4 v = r[2 * bj + n] + acc[ai][bj][m][n]; o[4 * bj + 2 * n] = cvt_pk_bf16(v[0], v[1]); o[4 * bj + 2 * n + 1] = cvt_pk_bf16(v[2], v[3]); }
;                 *(u32x4*)(out + off) = (u32x4){o[0], o[1], o[2], o[3]}; *(u32x4*)(out + off + 8) = (u32x4){o[4], o[5], o[6], o[7]}; }
.LBB0_477:
	v_lshl_add_u32 v6, s20, 8, v1
	v_lshl_or_b32 v4, s0, 8, v187
	v_readlane_b32 s44, v254, 14
	v_readlane_b32 s45, v254, 15
	v_readlane_b32 s0, v255, 11
	v_readlane_b32 s1, v255, 12
	s_andn2_b64 vcc, exec, s[2:3]
	v_readlane_b32 s46, v254, 16
	v_readlane_b32 s47, v254, 17
	v_readlane_b32 s48, v254, 18
	v_readlane_b32 s49, v254, 19
	v_readlane_b32 s50, v254, 20
	v_readlane_b32 s51, v254, 21
	v_readlane_b32 s52, v254, 22
	v_readlane_b32 s53, v254, 23
	v_readlane_b32 s54, v254, 24
	v_readlane_b32 s55, v254, 25
	v_readlane_b32 s56, v254, 26
	v_readlane_b32 s57, v254, 27
	v_readlane_b32 s58, v254, 28
	v_readlane_b32 s59, v254, 29
	v_lshl_add_u32 v178, v6, 10, v4
	v_lshlrev_b32_e32 v179, 2, v178
	v_lshlrev_b32_e32 v180, 1, v178
	s_nop 4
	global_load_dwordx4 v[2:5], v179, s[44:45]
	global_load_dwordx4 v[6:9], v179, s[44:45] offset:16
	global_load_dwordx4 v[10:13], v179, s[44:45] offset:32
	global_load_dwordx4 v[14:17], v179, s[44:45] offset:48
	v_add_u32_e32 v181, 0x10000, v179
	global_load_dwordx4 v[18:21], v181, s[44:45]
	global_load_dwordx4 v[22:25], v181, s[44:45] offset:16
	global_load_dwordx4 v[26:29], v181, s[44:45] offset:32
	global_load_dwordx4 v[30:33], v181, s[44:45] offset:48
	v_add_u32_e32 v182, 0x20000, v179
	global_load_dwordx4 v[194:197], v182, s[44:45]
	global_load_dwordx4 v[198:201], v182, s[44:45] offset:16
	global_load_dwordx4 v[202:205], v182, s[44:45] offset:32
	global_load_dwordx4 v[206:209], v182, s[44:45] offset:48
	v_add_u32_e32 v183, 0x30000, v179
	global_load_dwordx4 v[210:213], v183, s[44:45]
	global_load_dwordx4 v[214:217], v183, s[44:45] offset:16
	global_load_dwordx4 v[218:221], v183, s[44:45] offset:32
	global_load_dwordx4 v[222:225], v183, s[44:45] offset:48
	v_add_u32_e32 v184, 0x80000, v179
	global_load_dwordx4 v[228:231], v184, s[44:45]
	global_load_dwordx4 v[232:235], v184, s[44:45] offset:16
	global_load_dwordx4 v[236:239], v184, s[44:45] offset:32
	global_load_dwordx4 v[240:243], v184, s[44:45] offset:48
	s_waitcnt vmcnt(16)
	v_pk_add_f32 v[2:3], v[158:159], v[2:3]
	v_pk_add_f32 v[4:5], v[160:161], v[4:5]
	v_pk_add_f32 v[6:7], v[154:155], v[6:7]
	v_pk_add_f32 v[8:9], v[156:157], v[8:9]
	v_pk_add_f32 v[10:11], v[150:151], v[10:11]
	v_pk_add_f32 v[12:13], v[152:153], v[12:13]
	v_pk_add_f32 v[14:15], v[146:147], v[14:15]
	v_pk_add_f32 v[16:17], v[148:149], v[16:17]
	v_cvt_pk_bf16_f32 v2, v2, v3
	v_cvt_pk_bf16_f32 v3, v4, v5
	v_cvt_pk_bf16_f32 v4, v6, v7
	v_cvt_pk_bf16_f32 v5, v8, v9
	v_cvt_pk_bf16_f32 v6, v10, v11
	v_cvt_pk_bf16_f32 v7, v12, v13
	v_cvt_pk_bf16_f32 v8, v14, v15
	v_cvt_pk_bf16_f32 v9, v16, v17
	global_store_dwordx4 v180, v[2:5], s[0:1]
	global_store_dwordx4 v180, v[6:9], s[0:1] offset:16
	v_add_u32_e32 v181, 0x90000, v179
	global_load_dwordx4 v[146:149], v181, s[44:45]
	global_load_dwordx4 v[150:153], v181, s[44:45] offset:16
	global_load_dwordx4 v[154:157], v181, s[44:45] offset:32
	global_load_dwordx4 v[158:161], v181, s[44:45] offset:48
	s_waitcnt vmcnt(18)
	v_pk_add_f32 v[18:19], v[142:143], v[18:19]
	v_pk_add_f32 v[20:21], v[144:145], v[20:21]
	v_pk_add_f32 v[22:23], v[138:139], v[22:23]
	v_pk_add_f32 v[24:25], v[140:141], v[24:25]
	v_pk_add_f32 v[26:27], v[134:135], v[26:27]
	v_pk_add_f32 v[28:29], v[136:137], v[28:29]
	v_pk_add_f32 v[30:31], v[130:131], v[30:31]
	v_pk_add_f32 v[32:33], v[132:133], v[32:33]
	v_cvt_pk_bf16_f32 v18, v18, v19
	v_cvt_pk_bf16_f32 v19, v20, v21
	v_cvt_pk_bf16_f32 v20, v22, v23
	v_cvt_pk_bf16_f32 v21, v24, v25
	v_cvt_pk_bf16_f32 v22, v26, v27
	v_cvt_pk_bf16_f32 v23, v28, v29
	v_cvt_pk_bf16_f32 v24, v30, v31
	v_cvt_pk_bf16_f32 v25, v32, v33
	v_add_u32_e32 v185, 0x8000, v180
	global_store_dwordx4 v185, v[18:21], s[0:1]
	global_store_dwordx4 v185, v[22:25], s[0:1] offset:16
	v_add_u32_e32 v182, 0xa0000, v179
	global_load_dwordx4 v[130:133], v182, s[44:45]
	global_load_dwordx4 v[134:137], v182, s[44:45] offset:16
	global_load_dwordx4 v[138:141], v182, s[44:45] offset:32
	global_load_dwordx4 v[142:145], v182, s[44:45] offset:48
	s_waitcnt vmcnt(20)
	v_pk_add_f32 v[194:195], v[126:127], v[194:195]
	v_pk_add_f32 v[196:197], v[128:129], v[196:197]
	v_pk_add_f32 v[198:199], v[122:123], v[198:199]
	v_pk_add_f32 v[200:201], v[124:125], v[200:201]
	v_pk_add_f32 v[202:203], v[118:119], v[202:203]
	v_pk_add_f32 v[204:205], v[120:121], v[204:205]
	v_pk_add_f32 v[206:207], v[114:115], v[206:207]
	v_pk_add_f32 v[208:209], v[116:117], v[208:209]
	v_cvt_pk_bf16_f32 v194, v194, v195
	v_cvt_pk_bf16_f32 v195, v196, v197
	v_cvt_pk_bf16_f32 v196, v198, v199
	v_cvt_pk_bf16_f32 v197, v200, v201
	v_cvt_pk_bf16_f32 v198, v202, v203
	v_cvt_pk_bf16_f32 v199, v204, v205
	v_cvt_pk_bf16_f32 v200, v206, v207
	v_cvt_pk_bf16_f32 v201, v208, v209
	v_add_u32_e32 v185, 0x10000, v180
	global_store_dwordx4 v185, v[194:197], s[0:1]
	global_store_dwordx4 v185, v[198:201], s[0:1] offset:16
	v_add_u32_e32 v183, 0xb0000, v179
	global_load_dwordx4 v[114:117], v183, s[44:45]
	global_load_dwordx4 v[118:121], v183, s[44:45] offset:16
	global_load_dwordx4 v[122:125], v183, s[44:45] offset:32
	global_load_dwordx4 v[126:129], v183, s[44:45] offset:48
	s_waitcnt vmcnt(22)
;     ...
;         if (!has_next) break;
; #pragma unroll
;         for (int a = 0; a < 2; ++a)
; #pragma unroll
;             for (int b = 0; b < 2; ++b)
; #pragma unroll
;                 for (int m = 0; m < 4; ++m)
; #pragma unroll
;                     for (int n = 0; n < 2; ++n) acc[a][b][m][n] = (f32x4){0.f, 0.f, 0.f, 0.f};
;         cur = nxt; cA = nA; cB = nB; ++ui;
;     __device__ __forceinline__ void operator()(const f32x4 (&acc)[2][2][4][2], const Unit& u, int wr, int wc, int fr, int fq) const {
;         const int row0 = u.pm * BM + wr * 64 + fr, col0 = u.pn * BM + wc * 64 + 16 * fq;
; #pragma unroll
;         for (int ai = 0; ai < 2; ++ai)
; #pragma unroll
;             for (int m = 0; m < 4; ++m) { const size_t off = (size_t)(row0 + ai * HALF + m * 16) * ldc + col0;
;                 f32x4 r[4];
;                 if constexpr (RESID_F32) {
; #pragma unroll
;                     for (int p = 0; p < 4; ++p) r[p] = *(const f32x4*)((const float*)resid + off + 4 * p); }
;                 else { const u32x4 w0 = *(const u32x4*)((const bf16_t*)resid + off), w1 = *(const u32x4*)((const bf16_t*)resid + off + 8);
;                     r[0] = (f32x4){__uint_as_float(w0.x << 16), __uint_as_float(w0.x & 0xffff0000u), __uint_as_float(w0.y << 16), __uint_as_float(w0.y & 0xffff0000u)};
;                     r[1] = (f32x4){__uint_as_float(w0.z << 16), __uint_as_float(w0.z & 0xffff0000u), __uint_as_float(w0.w << 16), __uint_as_float(w0.w & 0xffff0000u)};
;                     r[2] = (f32x4){__uint_as_float(w1.x << 16), __uint_as_float(w1.x & 0xffff0000u), __uint_as_float(w1.y << 16), __uint_as_float(w1.y & 0xffff0000u)};
;                     r[3] = (f32x4){__uint_as_float(w1.z << 16), __uint_as_float(w1.z & 0xffff0000u), __uint_as_float(w1.w << 16), __uint_as_float(w1.w & 0xffff0000u)}; }
;                 unsigned o[8];
; #pragma unroll
;                 for (int bj = 0; bj < 2; ++bj)
; #pragma unroll
;                     for (int n = 0; n < 2; ++n) { const f32x4 v = r[2 * bj + n] + acc[ai][bj][m][n]; o[4 * bj + 2 * n] = cvt_pk_bf16(v[0], v[1]); o[4 * bj + 2 * n + 1] = cvt_pk_bf16(v[2], v[3]); }
;                 *(u32x4*)(out + off) = (u32x4){o[0], o[1], o[2], o[3]}; *(u32x4*)(out + off + 8) = (u32x4){o[4], o[5], o[6], o[7]}; }
	v_pk_add_f32 v[210:211], v[110:111], v[210:211]
	v_pk_add_f32 v[212:213], v[112:113], v[212:213]
	v_pk_add_f32 v[214:215], v[106:107], v[214:215]
	v_pk_add_f32 v[216:217], v[108:109], v[216:217]
	v_pk_add_f32 v[218:219], v[102:103], v[218:219]
	v_pk_add_f32 v[220:221], v[104:105], v[220:221]
	v_pk_add_f32 v[222:223], v[98:99], v[222:223]
	v_pk_add_f32 v[224:225], v[100:101], v[224:225]
	v_cvt_pk_bf16_f32 v210, v210, v211
	v_cvt_pk_bf16_f32 v211, v212, v213
	v_cvt_pk_bf16_f32 v212, v214, v215
	v_cvt_pk_bf16_f32 v213, v216, v217
	v_cvt_pk_bf16_f32 v214, v218, v219
	v_cvt_pk_bf16_f32 v215, v220, v221
	v_cvt_pk_bf16_f32 v216, v222, v223
	v_cvt_pk_bf16_f32 v217, v224, v225
	v_add_u32_e32 v185, 0x18000, v180
	global_store_dwordx4 v185, v[210:213], s[0:1]
	global_store_dwordx4 v185, v[214:217], s[0:1] offset:16
	s_waitcnt vmcnt(20)
	v_pk_add_f32 v[228:229], v[94:95], v[228:229]
	v_pk_add_f32 v[230:231], v[96:97], v[230:231]
	v_pk_add_f32 v[232:233], v[90:91], v[232:233]
	v_pk_add_f32 v[234:235], v[92:93], v[234:235]
	v_pk_add_f32 v[236:237], v[86:87], v[236:237]
	v_pk_add_f32 v[238:239], v[88:89], v[238:239]
	v_pk_add_f32 v[240:241], v[82:83], v[240:241]
	v_pk_add_f32 v[242:243], v[84:85], v[242:243]
	v_cvt_pk_bf16_f32 v228, v228, v229
	v_cvt_pk_bf16_f32 v229, v230, v231
	v_cvt_pk_bf16_f32 v230, v232, v233
	v_cvt_pk_bf16_f32 v231, v234, v235
	v_cvt_pk_bf16_f32 v232, v236, v237
	v_cvt_pk_bf16_f32 v233, v238, v239
	v_cvt_pk_bf16_f32 v234, v240, v241
	v_cvt_pk_bf16_f32 v235, v242, v243
	v_add_u32_e32 v185, 0x40000, v180
	global_store_dwordx4 v185, v[228:231], s[0:1]
	global_store_dwordx4 v185, v[232:235], s[0:1] offset:16
	s_waitcnt vmcnt(16)
	v_pk_add_f32 v[146:147], v[78:79], v[146:147]
	v_pk_add_f32 v[148:149], v[80:81], v[148:149]
	v_pk_add_f32 v[150:151], v[74:75], v[150:151]
	v_pk_add_f32 v[152:153], v[76:77], v[152:153]
	v_pk_add_f32 v[154:155], v[70:71], v[154:155]
	v_pk_add_f32 v[156:157], v[72:73], v[156:157]
	v_pk_add_f32 v[158:159], v[66:67], v[158:159]
	v_pk_add_f32 v[160:161], v[68:69], v[160:161]
	v_cvt_pk_bf16_f32 v146, v146, v147
	v_cvt_pk_bf16_f32 v147, v148, v149
	v_cvt_pk_bf16_f32 v148, v150, v151
	v_cvt_pk_bf16_f32 v149, v152, v153
	v_cvt_pk_bf16_f32 v150, v154, v155
	v_cvt_pk_bf16_f32 v151, v156, v157
	v_cvt_pk_bf16_f32 v152, v158, v159
	v_cvt_pk_bf16_f32 v153, v160, v161
	v_add_u32_e32 v185, 0x48000, v180
	global_store_dwordx4 v185, v[146:149], s[0:1]
	global_store_dwordx4 v185, v[150:153], s[0:1] offset:16
	s_waitcnt vmcnt(12)
	v_pk_add_f32 v[130:131], v[62:63], v[130:131]
	v_pk_add_f32 v[132:133], v[64:65], v[132:133]
	v_pk_add_f32 v[134:135], v[58:59], v[134:135]
	v_pk_add_f32 v[136:137], v[60:61], v[136:137]
	v_pk_add_f32 v[138:139], v[54:55], v[138:139]
	v_pk_add_f32 v[140:141], v[56:57], v[140:141]
	v_pk_add_f32 v[142:143], v[50:51], v[142:143]
	v_pk_add_f32 v[144:145], v[52:53], v[144:145]
	v_cvt_pk_bf16_f32 v130, v130, v131
	v_cvt_pk_bf16_f32 v131, v132, v133
	v_cvt_pk_bf16_f32 v132, v134, v135
	v_cvt_pk_bf16_f32 v133, v136, v137
	v_cvt_pk_bf16_f32 v134, v138, v139
	v_cvt_pk_bf16_f32 v135, v140, v141
	v_cvt_pk_bf16_f32 v136, v142, v143
	v_cvt_pk_bf16_f32 v137, v144, v145
	v_add_u32_e32 v185, 0x50000, v180
	global_store_dwordx4 v185, v[130:133], s[0:1]
	global_store_dwordx4 v185, v[134:137], s[0:1] offset:16
	s_waitcnt vmcnt(8)
	v_pk_add_f32 v[114:115], v[46:47], v[114:115]
	v_pk_add_f32 v[116:117], v[48:49], v[116:117]
	v_pk_add_f32 v[118:119], v[42:43], v[118:119]
	v_pk_add_f32 v[120:121], v[44:45], v[120:121]
	v_pk_add_f32 v[122:123], v[38:39], v[122:123]
	v_pk_add_f32 v[124:125], v[40:41], v[124:125]
	v_pk_add_f32 v[126:127], v[34:35], v[126:127]
	v_pk_add_f32 v[128:129], v[36:37], v[128:129]
	v_cvt_pk_bf16_f32 v114, v114, v115
	v_cvt_pk_bf16_f32 v115, v116, v117
	v_cvt_pk_bf16_f32 v116, v118, v119
	v_cvt_pk_bf16_f32 v117, v120, v121
	v_cvt_pk_bf16_f32 v118, v122, v123
	v_cvt_pk_bf16_f32 v119, v124, v125
	v_cvt_pk_bf16_f32 v120, v126, v127
	v_cvt_pk_bf16_f32 v121, v128, v129
	v_add_u32_e32 v185, 0x58000, v180
	global_store_dwordx4 v185, v[114:117], s[0:1]
	global_store_dwordx4 v185, v[118:121], s[0:1] offset:16
	s_mov_b64 s[20:21], 0x20000
	s_mov_b64 s[20:21], 0x24000
	s_mov_b64 s[20:21], 0x28000
	s_mov_b64 s[20:21], 0x2c000
	s_mov_b64 s[20:21], -1
	s_cbranch_vccnz .LBB0_466
	s_andn2_b64 vcc, exec, s[6:7]
	s_cbranch_vccnz .LBB0_465
	s_barrier
	s_branch .LBB0_465

; #define PG8_STAGE(bufoff, gbase, voff) do { _Pragma("unroll") for (int _i = 0; _i < 2; ++_i) \
;         __builtin_amdgcn_global_load_lds((const unsigned*)((const char*)(gbase) + (voff)[_i]), (PG8_LAS unsigned*)(lds + (bufoff) + ldsw + _i * 8192), 16, 0, 0); } while (0)
; #define PG8_STAGE_A(bufoff, gbase, h, nx) do { if constexpr (Sched::GATHER) { const unsigned vv_[2] = {(nx) ? vAn[h][0] : vA[h][0], (nx) ? vAn[h][1] : vA[h][1]}; PG8_STAGE(bufoff, gbase, vv_); } \
;         else { PG8_STAGE(bufoff, (gbase) + (h) * hstep, voffA); } } while (0)
; #define PG8_LDA(dst, b, h) do { _Pragma("unroll") for (int m = 0; m < 4; ++m) _Pragma("unroll") for (int k = 0; k < 2; ++k) dst[m][k] = *(const PG8_LAS bf16x8*)(lds + PG8_SA(b, h) + aoff + m * 2048 + k * 1024); } while (0)
; #define PG8_WAIT_V(n) asm volatile("s_waitcnt vmcnt(" #n ")" ::: "memory")
; #define PG8_WAIT_L(n) asm volatile("s_waitcnt lgkmcnt(" #n ")" ::: "memory")
;     ...
;         const bool has_next = S.next(ui + 1, nxt);
;         const char* nA = Sched::GATHER ? cA : (has_next ? (const char*)g.A + (size_t)nxt.pm * tstep : cA);
;         if constexpr (Sched::GATHER) { if (has_next) { PG8_AOFF(vAn, ui + 1); } else { _Pragma("unroll") for (int h_ = 0; h_ < 2; ++h_) _Pragma("unroll") for (int i_ = 0; i_ < 2; ++i_) vAn[h_][i_] = vA[h_][i_]; } } const char* nB = has_next ? (const char*)g.Bt + (size_t)nxt.pb * tstep : cB;
; #pragma nounroll
;         for (int t = 0; t < nt; t += 2) {
;             const bool last = (t == nt - 2);
;             const char* a1 = cA + (size_t)(t + 1) * kstep;
;             const char* a2 = last ? nA : cA + (size_t)(t + 2) * kstep; const char* b2 = last ? nB : cB + (size_t)(t + 2) * kstep;
;             const char* a3 = a2 + kstep; const char* b3 = b2 + kstep;
;             if (last && has_next) S.a_ready(nxt);
;             if constexpr (SP2) {
;             PG8_LDB(B0, 0, 0); PG8_LDB(B1, 0, 1); PG8_SCHED; PG8_LDA(At, 0, 0); PG8_STAGE_A(PG8_SA(1, 1), a1, 1, false);
;             PG8_WAIT_V(8); PG8_WAIT_L(0); PG8_BAR; PG8_MMA(0, 0, At, B0); PG8_MMA(0, 1, At, B1); PG8_BAR; PG8_SCHED;
;             PG8_LDA(At, 0, 1); PG8_STAGE(PG8_SB(0, 0), b2, voffB); PG8_STAGE(PG8_SB(0, 1), b2 + hstepB, voffB); PG8_STAGE_A(PG8_SA(0, 0), a2, 0, last);
;             PG8_WAIT_V(8); PG8_WAIT_L(0); PG8_BAR; PG8_MMA(1, 0, At, B0); PG8_MMA(1, 1, At, B1); PG8_BAR; PG8_SCHED;
.LBB0_1204:
	s_ashr_i32 s17, s16, 31
	s_lshl_b64 s[18:19], s[16:17], 18
	v_readlane_b32 s20, v255, 21
	v_readlane_b32 s21, v255, 22
	s_add_u32 s18, s20, s18
	s_addc_u32 s19, s21, s19
	s_and_b64 s[20:21], s[2:3], exec
	s_cselect_b32 s17, s19, s25
	s_cselect_b32 s44, s18, s24
	s_ashr_i32 s15, s14, 31
	s_lshl_b64 s[20:21], s[14:15], 18
	v_readlane_b32 s28, v254, 57
	v_readlane_b32 s29, v254, 58
	s_add_u32 s20, s28, s20
	s_addc_u32 s21, s29, s21
	s_and_b64 s[28:29], s[2:3], exec
	s_cselect_b32 s15, s21, s27
	s_cselect_b32 s45, s20, s26
	s_add_u32 s24, s24, 0x20080
	s_addc_u32 s25, s25, 0
	s_add_u32 s46, s26, 0x100
	s_addc_u32 s47, s27, 0
	s_mov_b32 s48, -2
	ds_read_b128 v[26:29], v188
	ds_read_b128 v[30:33], v188 offset:1024
	ds_read_b128 v[18:21], v188 offset:2048
	ds_read_b128 v[22:25], v188 offset:3072
	ds_read_b128 v[10:13], v189
	ds_read_b128 v[14:17], v189 offset:1024
	ds_read_b128 v[2:5], v189 offset:2048
	ds_read_b128 v[6:9], v189 offset:3072
	s_add_u32 s26, s24, 0xfffe0080
	s_addc_u32 s27, s25, -1
	s_cmp_eq_u32 s48, 4
	s_cselect_b32 s29, s17, s27
	s_cselect_b32 s28, s44, s26
	s_cselect_b32 s27, s15, s47
	s_cselect_b32 s26, s45, s46
	v_lshl_add_u64 v[218:219], s[24:25], 0, v[170:171]
	s_add_i32 m0, s23, 0xc000
	ds_read_b128 v[178:181], v190
	ds_read_b128 v[182:185], v190 offset:1024
	ds_read_b128 v[194:197], v190 offset:2048
	ds_read_b128 v[198:201], v190 offset:3072
	ds_read_b128 v[202:205], v190 offset:4096
	ds_read_b128 v[206:209], v190 offset:5120
	ds_read_b128 v[210:213], v190 offset:6144
	ds_read_b128 v[214:217], v190 offset:7168
	global_load_lds_dwordx4 v[218:219], off
	v_lshl_add_u64 v[218:219], s[24:25], 0, v[172:173]
	s_add_i32 m0, s23, 0xe000
	s_nop 0
	global_load_lds_dwordx4 v[218:219], off
	s_waitcnt vmcnt(8)
	s_waitcnt lgkmcnt(0)
	s_barrier
	s_setprio 1
	s_nop 3
	s_waitcnt lgkmcnt(0)
	v_mfma_scale_f32_16x16x128_f8f6f4 v[158:161], v[26:33], v[178:185], 0, v191, v192 op_sel_hi:[0,0,0]
	v_mfma_scale_f32_16x16x128_f8f6f4 v[154:157], v[18:25], v[178:185], 0, v191, v192 op_sel_hi:[0,0,0]
	v_mfma_scale_f32_16x16x128_f8f6f4 v[142:145], v[26:33], v[194:201], 0, v191, v192 op_sel_hi:[0,0,0]
	v_mfma_scale_f32_16x16x128_f8f6f4 v[138:141], v[18:25], v[194:201], 0, v191, v192 op_sel_hi:[0,0,0]
	v_mfma_scale_f32_16x16x128_f8f6f4 v[126:129], v[26:33], v[202:209], 0, v191, v192 op_sel_hi:[0,0,0]
	v_mfma_scale_f32_16x16x128_f8f6f4 v[122:125], v[18:25], v[202:209], 0, v191, v192 op_sel_hi:[0,0,0]
	v_mfma_scale_f32_16x16x128_f8f6f4 v[110:113], v[26:33], v[210:217], 0, v191, v192 op_sel_hi:[0,0,0]
	v_mfma_scale_f32_16x16x128_f8f6f4 v[106:109], v[18:25], v[210:217], 0, v191, v192 op_sel_hi:[0,0,0]
	s_setprio 0
	s_setprio 1
	s_nop 3
	v_mfma_scale_f32_16x16x128_f8f6f4 v[150:153], v[10:17], v[178:185], 0, v191, v192 op_sel_hi:[0,0,0]
	v_mfma_scale_f32_16x16x128_f8f6f4 v[146:149], v[2:9], v[178:185], 0, v191, v192 op_sel_hi:[0,0,0]
	v_mfma_scale_f32_16x16x128_f8f6f4 v[134:137], v[10:17], v[194:201], 0, v191, v192 op_sel_hi:[0,0,0]
	v_mfma_scale_f32_16x16x128_f8f6f4 v[130:133], v[2:9], v[194:201], 0, v191, v192 op_sel_hi:[0,0,0]
	v_mfma_scale_f32_16x16x128_f8f6f4 v[118:121], v[10:17], v[202:209], 0, v191, v192 op_sel_hi:[0,0,0]
	v_mfma_scale_f32_16x16x128_f8f6f4 v[114:117], v[2:9], v[202:209], 0, v191, v192 op_sel_hi:[0,0,0]
	v_mfma_scale_f32_16x16x128_f8f6f4 v[102:105], v[10:17], v[210:217], 0, v191, v192 op_sel_hi:[0,0,0]
	v_mfma_scale_f32_16x16x128_f8f6f4 v[98:101], v[2:9], v[210:217], 0, v191, v192 op_sel_hi:[0,0,0]
	s_setprio 0
	s_barrier
	s_add_i32 s49, s41, s30
	v_lshl_add_u64 v[178:179], s[26:27], 0, v[164:165]
	s_mov_b32 m0, s49
	ds_read_b128 v[194:197], v190 offset:16384
	ds_read_b128 v[198:201], v190 offset:17408
	ds_read_b128 v[202:205], v190 offset:18432
	ds_read_b128 v[206:209], v190 offset:19456
	ds_read_b128 v[210:213], v190 offset:20480
	ds_read_b128 v[214:217], v190 offset:21504
	ds_read_b128 v[218:221], v190 offset:22528
	ds_read_b128 v[222:225], v190 offset:23552
	global_load_lds_dwordx4 v[178:179], off
	s_add_i32 m0, s49, 0x2000
	s_add_u32 s50, s26, 0x2000
	v_lshl_add_u64 v[180:181], s[26:27], 0, v[168:169]
	s_addc_u32 s51, s27, 0
	s_add_i32 s49, s42, s30
	global_load_lds_dwordx4 v[180:181], off
	v_lshl_add_u64 v[182:183], s[50:51], 0, v[164:165]
	s_mov_b32 m0, s49
	v_lshl_add_u64 v[184:185], s[28:29], 0, v[166:167]
	global_load_lds_dwordx4 v[182:183], off
	v_lshl_add_u64 v[182:183], s[50:51], 0, v[168:169]
	s_add_i32 m0, s49, 0x2000
	s_nop 0
	global_load_lds_dwordx4 v[182:183], off
	v_lshl_add_u64 v[182:183], s[28:29], 0, v[162:163]
	s_mov_b32 m0, s23
	s_nop 0
	global_load_lds_dwordx4 v[182:183], off
	s_mov_b32 m0, s34
	s_nop 0
	global_load_lds_dwordx4 v[184:185], off
	s_waitcnt vmcnt(8)
	s_waitcnt lgkmcnt(0)
	s_barrier
	s_setprio 1
	s_nop 3
	s_waitcnt lgkmcnt(0)
	v_mfma_scale_f32_16x16x128_f8f6f4 v[94:97], v[26:33], v[194:201], 0, v191, v192 op_sel_hi:[0,0,0]
	v_mfma_scale_f32_16x16x128_f8f6f4 v[90:93], v[18:25], v[194:201], 0, v191, v192 op_sel_hi:[0,0,0]
	v_mfma_scale_f32_16x16x128_f8f6f4 v[78:81], v[26:33], v[202:209], 0, v191, v192 op_sel_hi:[0,0,0]
	v_mfma_scale_f32_16x16x128_f8f6f4 v[74:77], v[18:25], v[202:209], 0, v191, v192 op_sel_hi:[0,0,0]
	v_mfma_scale_f32_16x16x128_f8f6f4 v[62:65], v[26:33], v[210:217], 0, v191, v192 op_sel_hi:[0,0,0]
	v_mfma_scale_f32_16x16x128_f8f6f4 v[58:61], v[18:25], v[210:217], 0, v191, v192 op_sel_hi:[0,0,0]
	v_mfma_scale_f32_16x16x128_f8f6f4 v[46:49], v[26:33], v[218:225], 0, v191, v192 op_sel_hi:[0,0,0]
	v_mfma_scale_f32_16x16x128_f8f6f4 v[42:45], v[18:25], v[218:225], 0, v191, v192 op_sel_hi:[0,0,0]
	s_setprio 0
	s_setprio 1
	s_nop 3
	v_mfma_scale_f32_16x16x128_f8f6f4 v[86:89], v[10:17], v[194:201], 0, v191, v192 op_sel_hi:[0,0,0]
	v_mfma_scale_f32_16x16x128_f8f6f4 v[82:85], v[2:9], v[194:201], 0, v191, v192 op_sel_hi:[0,0,0]
	v_mfma_scale_f32_16x16x128_f8f6f4 v[70:73], v[10:17], v[202:209], 0, v191, v192 op_sel_hi:[0,0,0]
	v_mfma_scale_f32_16x16x128_f8f6f4 v[66:69], v[2:9], v[202:209], 0, v191, v192 op_sel_hi:[0,0,0]
	v_mfma_scale_f32_16x16x128_f8f6f4 v[54:57], v[10:17], v[210:217], 0, v191, v192 op_sel_hi:[0,0,0]
	v_mfma_scale_f32_16x16x128_f8f6f4 v[50:53], v[2:9], v[210:217], 0, v191, v192 op_sel_hi:[0,0,0]
	v_mfma_scale_f32_16x16x128_f8f6f4 v[38:41], v[10:17], v[218:225], 0, v191, v192 op_sel_hi:[0,0,0]
	v_mfma_scale_f32_16x16x128_f8f6f4 v[34:37], v[2:9], v[218:225], 0, v191, v192 op_sel_hi:[0,0,0]
	s_setprio 0
	s_barrier
; #define PG8_STAGE(bufoff, gbase, voff) do { _Pragma("unroll") for (int _i = 0; _i < 2; ++_i) \
;         __builtin_amdgcn_global_load_lds((const unsigned*)((const char*)(gbase) + (voff)[_i]), (PG8_LAS unsigned*)(lds + (bufoff) + ldsw + _i * 8192), 16, 0, 0); } while (0)
; #define PG8_STAGE_A(bufoff, gbase, h, nx) do { if constexpr (Sched::GATHER) { const unsigned vv_[2] = {(nx) ? vAn[h][0] : vA[h][0], (nx) ? vAn[h][1] : vA[h][1]}; PG8_STAGE(bufoff, gbase, vv_); } \
;         else { PG8_STAGE(bufoff, (gbase) + (h) * hstep, voffA); } } while (0)
; #define PG8_LDA(dst, b, h) do { _Pragma("unroll") for (int m = 0; m < 4; ++m) _Pragma("unroll") for (int k = 0; k < 2; ++k) dst[m][k] = *(const PG8_LAS bf16x8*)(lds + PG8_SA(b, h) + aoff + m * 2048 + k * 1024); } while (0)
; #define PG8_LDB(dst, b, h) do { _Pragma("unroll") for (int n = 0; n < 2; ++n) _Pragma("unroll") for (int k = 0; k < 2; ++k) dst[n][k] = *(const PG8_LAS bf16x8*)(lds + PG8_SB(b, h) + boff + n * 2048 + k * 1024); } while (0)
; #define PG8_WAIT_V(n) asm volatile("s_waitcnt vmcnt(" #n ")" ::: "memory")
; #define PG8_WAIT_L(n) asm volatile("s_waitcnt lgkmcnt(" #n ")" ::: "memory")
; #define PG8_BAR __builtin_amdgcn_s_barrier()
; #define PG8_SCHED __builtin_amdgcn_sched_barrier(0)
;     ...
;             PG8_LDB(B0, 1, 0); PG8_LDB(B1, 1, 1); PG8_SCHED; PG8_LDA(At, 1, 0); PG8_STAGE_A(PG8_SA(0, 1), a2, 1, last);
;             PG8_WAIT_V(8); PG8_WAIT_L(0); PG8_BAR; PG8_MMA(0, 0, At, B0); PG8_MMA(0, 1, At, B1); PG8_BAR; PG8_SCHED;
;             PG8_LDA(At, 1, 1); PG8_STAGE(PG8_SB(1, 0), b3, voffB); PG8_STAGE(PG8_SB(1, 1), b3 + hstepB, voffB); PG8_STAGE_A(PG8_SA(1, 0), a3, 0, last);
;             PG8_WAIT_V(8); PG8_WAIT_L(0); PG8_BAR; PG8_MMA(1, 0, At, B0); PG8_MMA(1, 1, At, B1); PG8_BAR; PG8_SCHED;
	s_add_i32 s49, 0, 0x18000
	s_add_i32 s50, 0, 0x1c000
	v_add_u32_e32 v14, s49, v186
	v_add_u32_e32 v30, s50, v186
	ds_read_b128 v[2:5], v14
	ds_read_b128 v[6:9], v14 offset:1024
	ds_read_b128 v[10:13], v14 offset:2048
	ds_read_b128 v[14:17], v14 offset:3072
	ds_read_b128 v[18:21], v30
	ds_read_b128 v[22:25], v30 offset:1024
	ds_read_b128 v[26:29], v30 offset:2048
	ds_read_b128 v[30:33], v30 offset:3072
	s_add_u32 s28, s28, 0x20000
	s_addc_u32 s29, s29, 0
	s_mov_b32 m0, s35
	v_lshl_add_u64 v[226:227], s[28:29], 0, v[162:163]
	ds_read_b128 v[194:197], v190 offset:32768
	ds_read_b128 v[198:201], v190 offset:33792
	ds_read_b128 v[202:205], v190 offset:34816
	ds_read_b128 v[206:209], v190 offset:35840
	ds_read_b128 v[210:213], v190 offset:36864
	ds_read_b128 v[214:217], v190 offset:37888
	ds_read_b128 v[218:221], v190 offset:38912
	ds_read_b128 v[222:225], v190 offset:39936
	global_load_lds_dwordx4 v[226:227], off
	v_lshl_add_u64 v[226:227], s[28:29], 0, v[166:167]
	s_mov_b32 m0, s36
	s_nop 0
	global_load_lds_dwordx4 v[226:227], off
	s_waitcnt vmcnt(8)
	s_waitcnt lgkmcnt(0)
	s_barrier
	s_setprio 1
	s_nop 3
	s_waitcnt lgkmcnt(0)
	v_mfma_scale_f32_16x16x128_f8f6f4 v[158:161], v[2:9], v[194:201], v[158:161], v191, v192 op_sel_hi:[0,0,0]
	v_mfma_scale_f32_16x16x128_f8f6f4 v[154:157], v[10:17], v[194:201], v[154:157], v191, v192 op_sel_hi:[0,0,0]
	v_mfma_scale_f32_16x16x128_f8f6f4 v[142:145], v[2:9], v[202:209], v[142:145], v191, v192 op_sel_hi:[0,0,0]
	v_mfma_scale_f32_16x16x128_f8f6f4 v[138:141], v[10:17], v[202:209], v[138:141], v191, v192 op_sel_hi:[0,0,0]
	v_mfma_scale_f32_16x16x128_f8f6f4 v[126:129], v[2:9], v[210:217], v[126:129], v191, v192 op_sel_hi:[0,0,0]
	v_mfma_scale_f32_16x16x128_f8f6f4 v[122:125], v[10:17], v[210:217], v[122:125], v191, v192 op_sel_hi:[0,0,0]
	v_mfma_scale_f32_16x16x128_f8f6f4 v[110:113], v[2:9], v[218:225], v[110:113], v191, v192 op_sel_hi:[0,0,0]
	v_mfma_scale_f32_16x16x128_f8f6f4 v[106:109], v[10:17], v[218:225], v[106:109], v191, v192 op_sel_hi:[0,0,0]
	s_setprio 0
	s_setprio 1
	s_nop 3
	v_mfma_scale_f32_16x16x128_f8f6f4 v[150:153], v[18:25], v[194:201], v[150:153], v191, v192 op_sel_hi:[0,0,0]
	v_mfma_scale_f32_16x16x128_f8f6f4 v[146:149], v[26:33], v[194:201], v[146:149], v191, v192 op_sel_hi:[0,0,0]
	v_mfma_scale_f32_16x16x128_f8f6f4 v[134:137], v[18:25], v[202:209], v[134:137], v191, v192 op_sel_hi:[0,0,0]
	v_mfma_scale_f32_16x16x128_f8f6f4 v[130:133], v[26:33], v[202:209], v[130:133], v191, v192 op_sel_hi:[0,0,0]
	v_mfma_scale_f32_16x16x128_f8f6f4 v[118:121], v[18:25], v[210:217], v[118:121], v191, v192 op_sel_hi:[0,0,0]
	v_mfma_scale_f32_16x16x128_f8f6f4 v[114:117], v[26:33], v[210:217], v[114:117], v191, v192 op_sel_hi:[0,0,0]
	v_mfma_scale_f32_16x16x128_f8f6f4 v[102:105], v[18:25], v[218:225], v[102:105], v191, v192 op_sel_hi:[0,0,0]
	v_mfma_scale_f32_16x16x128_f8f6f4 v[98:101], v[26:33], v[218:225], v[98:101], v191, v192 op_sel_hi:[0,0,0]
	s_setprio 0
	s_barrier
	s_add_i32 s28, s49, s30
	v_lshl_add_u64 v[178:179], v[178:179], 0, s[8:9]
	s_mov_b32 m0, s28
	ds_read_b128 v[194:197], v190 offset:49152
	ds_read_b128 v[198:201], v190 offset:50176
	ds_read_b128 v[202:205], v190 offset:51200
	ds_read_b128 v[206:209], v190 offset:52224
	ds_read_b128 v[210:213], v190 offset:53248
	ds_read_b128 v[214:217], v190 offset:54272
	ds_read_b128 v[218:221], v190 offset:55296
	ds_read_b128 v[222:225], v190 offset:56320
	global_load_lds_dwordx4 v[178:179], off
	s_add_i32 m0, s28, 0x2000
	s_add_u32 s26, s26, 0x2080
	v_lshl_add_u64 v[178:179], v[180:181], 0, s[8:9]
	s_addc_u32 s27, s27, 0
	s_add_i32 s28, s50, s30
	global_load_lds_dwordx4 v[178:179], off
	v_lshl_add_u64 v[178:179], s[26:27], 0, v[164:165]
	s_mov_b32 m0, s28
	s_nop 0
	global_load_lds_dwordx4 v[178:179], off
	v_lshl_add_u64 v[178:179], s[26:27], 0, v[168:169]
	s_add_i32 m0, s28, 0x2000
	s_nop 0
	global_load_lds_dwordx4 v[178:179], off
	v_lshl_add_u64 v[178:179], v[182:183], 0, s[8:9]
	s_mov_b32 m0, s39
	s_nop 0
	global_load_lds_dwordx4 v[178:179], off
	v_lshl_add_u64 v[178:179], v[184:185], 0, s[8:9]
	s_mov_b32 m0, s40
	s_nop 0
	global_load_lds_dwordx4 v[178:179], off
	s_waitcnt vmcnt(8)
	s_waitcnt lgkmcnt(0)
	s_barrier
	s_setprio 1
	s_nop 3
	s_waitcnt lgkmcnt(0)
	v_mfma_scale_f32_16x16x128_f8f6f4 v[94:97], v[2:9], v[194:201], v[94:97], v191, v192 op_sel_hi:[0,0,0]
	v_mfma_scale_f32_16x16x128_f8f6f4 v[90:93], v[10:17], v[194:201], v[90:93], v191, v192 op_sel_hi:[0,0,0]
	v_mfma_scale_f32_16x16x128_f8f6f4 v[78:81], v[2:9], v[202:209], v[78:81], v191, v192 op_sel_hi:[0,0,0]
	v_mfma_scale_f32_16x16x128_f8f6f4 v[74:77], v[10:17], v[202:209], v[74:77], v191, v192 op_sel_hi:[0,0,0]
	v_mfma_scale_f32_16x16x128_f8f6f4 v[62:65], v[2:9], v[210:217], v[62:65], v191, v192 op_sel_hi:[0,0,0]
	v_mfma_scale_f32_16x16x128_f8f6f4 v[58:61], v[10:17], v[210:217], v[58:61], v191, v192 op_sel_hi:[0,0,0]
	v_mfma_scale_f32_16x16x128_f8f6f4 v[46:49], v[2:9], v[218:225], v[46:49], v191, v192 op_sel_hi:[0,0,0]
	v_mfma_scale_f32_16x16x128_f8f6f4 v[42:45], v[10:17], v[218:225], v[42:45], v191, v192 op_sel_hi:[0,0,0]
	s_setprio 0
	s_setprio 1
	s_nop 3
	v_mfma_scale_f32_16x16x128_f8f6f4 v[86:89], v[18:25], v[194:201], v[86:89], v191, v192 op_sel_hi:[0,0,0]
	v_mfma_scale_f32_16x16x128_f8f6f4 v[82:85], v[26:33], v[194:201], v[82:85], v191, v192 op_sel_hi:[0,0,0]
	v_mfma_scale_f32_16x16x128_f8f6f4 v[70:73], v[18:25], v[202:209], v[70:73], v191, v192 op_sel_hi:[0,0,0]
	v_mfma_scale_f32_16x16x128_f8f6f4 v[66:69], v[26:33], v[202:209], v[66:69], v191, v192 op_sel_hi:[0,0,0]
	v_mfma_scale_f32_16x16x128_f8f6f4 v[54:57], v[18:25], v[210:217], v[54:57], v191, v192 op_sel_hi:[0,0,0]
	v_mfma_scale_f32_16x16x128_f8f6f4 v[50:53], v[26:33], v[210:217], v[50:53], v191, v192 op_sel_hi:[0,0,0]
	v_mfma_scale_f32_16x16x128_f8f6f4 v[38:41], v[18:25], v[218:225], v[38:41], v191, v192 op_sel_hi:[0,0,0]
	v_mfma_scale_f32_16x16x128_f8f6f4 v[34:37], v[26:33], v[218:225], v[34:37], v191, v192 op_sel_hi:[0,0,0]
	s_setprio 0
	s_barrier
	s_add_i32 s48, s48, 2
	s_add_u32 s24, s24, 0x100
	s_addc_u32 s25, s25, 0
	s_add_u32 s46, s46, 0x100
	s_addc_u32 s47, s47, 0
; #define PG8_STAGE(bufoff, gbase, voff) do { _Pragma("unroll") for (int _i = 0; _i < 2; ++_i) \
;         __builtin_amdgcn_global_load_lds((const unsigned*)((const char*)(gbase) + (voff)[_i]), (PG8_LAS unsigned*)(lds + (bufoff) + ldsw + _i * 8192), 16, 0, 0); } while (0)
; #define PG8_STAGE_A(bufoff, gbase, h, nx) do { if constexpr (Sched::GATHER) { const unsigned vv_[2] = {(nx) ? vAn[h][0] : vA[h][0], (nx) ? vAn[h][1] : vA[h][1]}; PG8_STAGE(bufoff, gbase, vv_); } \
;         else { PG8_STAGE(bufoff, (gbase) + (h) * hstep, voffA); } } while (0)
; #define PG8_LDA(dst, b, h) do { _Pragma("unroll") for (int m = 0; m < 4; ++m) _Pragma("unroll") for (int k = 0; k < 2; ++k) dst[m][k] = *(const PG8_LAS bf16x8*)(lds + PG8_SA(b, h) + aoff + m * 2048 + k * 1024); } while (0)
; #define PG8_LDB(dst, b, h) do { _Pragma("unroll") for (int n = 0; n < 2; ++n) _Pragma("unroll") for (int k = 0; k < 2; ++k) dst[n][k] = *(const PG8_LAS bf16x8*)(lds + PG8_SB(b, h) + boff + n * 2048 + k * 1024); } while (0)
; #define PG8_WAIT_V(n) asm volatile("s_waitcnt vmcnt(" #n ")" ::: "memory")
; #define PG8_WAIT_L(n) asm volatile("s_waitcnt lgkmcnt(" #n ")" ::: "memory")
; #define PG8_BAR __builtin_amdgcn_s_barrier()
; #define PG8_SCHED __builtin_amdgcn_sched_barrier(0)
;     ...
;             PG8_LDB(B0, 0, 0); PG8_LDB(B1, 0, 1); PG8_SCHED; PG8_LDA(At, 0, 0); PG8_STAGE_A(PG8_SA(1, 1), a1, 1, false);
;             PG8_WAIT_V(8); PG8_WAIT_L(0); PG8_BAR; PG8_MMA(0, 0, At, B0); PG8_MMA(0, 1, At, B1); PG8_BAR; PG8_SCHED;
;             PG8_LDA(At, 0, 1); PG8_STAGE(PG8_SB(0, 0), b2, voffB); PG8_STAGE(PG8_SB(0, 1), b2 + hstepB, voffB); PG8_STAGE_A(PG8_SA(0, 0), a2, 0, last);
;             PG8_WAIT_V(8); PG8_WAIT_L(0); PG8_BAR; PG8_MMA(1, 0, At, B0); PG8_MMA(1, 1, At, B1); PG8_BAR; PG8_SCHED;
.LBB0_1205:
	ds_read_b128 v[26:29], v188
	ds_read_b128 v[30:33], v188 offset:1024
	ds_read_b128 v[18:21], v188 offset:2048
	ds_read_b128 v[22:25], v188 offset:3072
	ds_read_b128 v[10:13], v189
	ds_read_b128 v[14:17], v189 offset:1024
	ds_read_b128 v[2:5], v189 offset:2048
	ds_read_b128 v[6:9], v189 offset:3072
	s_add_u32 s26, s24, 0xfffe0080
	s_addc_u32 s27, s25, -1
	s_cmp_eq_u32 s48, 4
	s_cselect_b32 s29, s17, s27
	s_cselect_b32 s28, s44, s26
	s_cselect_b32 s27, s15, s47
	s_cselect_b32 s26, s45, s46
	v_lshl_add_u64 v[218:219], s[24:25], 0, v[170:171]
	s_add_i32 m0, s23, 0xc000
	ds_read_b128 v[178:181], v190
	ds_read_b128 v[182:185], v190 offset:1024
	ds_read_b128 v[194:197], v190 offset:2048
	ds_read_b128 v[198:201], v190 offset:3072
	ds_read_b128 v[202:205], v190 offset:4096
	ds_read_b128 v[206:209], v190 offset:5120
	ds_read_b128 v[210:213], v190 offset:6144
	ds_read_b128 v[214:217], v190 offset:7168
	global_load_lds_dwordx4 v[218:219], off
	v_lshl_add_u64 v[218:219], s[24:25], 0, v[172:173]
	s_add_i32 m0, s23, 0xe000
	s_nop 0
	global_load_lds_dwordx4 v[218:219], off
	s_waitcnt vmcnt(8)
	s_waitcnt lgkmcnt(0)
	s_barrier
	s_setprio 1
	s_nop 3
	s_waitcnt lgkmcnt(0)
	v_mfma_scale_f32_16x16x128_f8f6f4 v[158:161], v[26:33], v[178:185], v[158:161], v191, v192 op_sel_hi:[0,0,0]
	v_mfma_scale_f32_16x16x128_f8f6f4 v[154:157], v[18:25], v[178:185], v[154:157], v191, v192 op_sel_hi:[0,0,0]
	v_mfma_scale_f32_16x16x128_f8f6f4 v[142:145], v[26:33], v[194:201], v[142:145], v191, v192 op_sel_hi:[0,0,0]
	v_mfma_scale_f32_16x16x128_f8f6f4 v[138:141], v[18:25], v[194:201], v[138:141], v191, v192 op_sel_hi:[0,0,0]
	v_mfma_scale_f32_16x16x128_f8f6f4 v[126:129], v[26:33], v[202:209], v[126:129], v191, v192 op_sel_hi:[0,0,0]
	v_mfma_scale_f32_16x16x128_f8f6f4 v[122:125], v[18:25], v[202:209], v[122:125], v191, v192 op_sel_hi:[0,0,0]
	v_mfma_scale_f32_16x16x128_f8f6f4 v[110:113], v[26:33], v[210:217], v[110:113], v191, v192 op_sel_hi:[0,0,0]
	v_mfma_scale_f32_16x16x128_f8f6f4 v[106:109], v[18:25], v[210:217], v[106:109], v191, v192 op_sel_hi:[0,0,0]
	s_setprio 0
	s_setprio 1
	s_nop 3
	v_mfma_scale_f32_16x16x128_f8f6f4 v[150:153], v[10:17], v[178:185], v[150:153], v191, v192 op_sel_hi:[0,0,0]
	v_mfma_scale_f32_16x16x128_f8f6f4 v[146:149], v[2:9], v[178:185], v[146:149], v191, v192 op_sel_hi:[0,0,0]
	v_mfma_scale_f32_16x16x128_f8f6f4 v[134:137], v[10:17], v[194:201], v[134:137], v191, v192 op_sel_hi:[0,0,0]
	v_mfma_scale_f32_16x16x128_f8f6f4 v[130:133], v[2:9], v[194:201], v[130:133], v191, v192 op_sel_hi:[0,0,0]
	v_mfma_scale_f32_16x16x128_f8f6f4 v[118:121], v[10:17], v[202:209], v[118:121], v191, v192 op_sel_hi:[0,0,0]
	v_mfma_scale_f32_16x16x128_f8f6f4 v[114:117], v[2:9], v[202:209], v[114:117], v191, v192 op_sel_hi:[0,0,0]
	v_mfma_scale_f32_16x16x128_f8f6f4 v[102:105], v[10:17], v[210:217], v[102:105], v191, v192 op_sel_hi:[0,0,0]
	v_mfma_scale_f32_16x16x128_f8f6f4 v[98:101], v[2:9], v[210:217], v[98:101], v191, v192 op_sel_hi:[0,0,0]
	s_setprio 0
	s_barrier
	s_add_i32 s49, s41, s30
	v_lshl_add_u64 v[178:179], s[26:27], 0, v[164:165]
	s_mov_b32 m0, s49
	ds_read_b128 v[194:197], v190 offset:16384
	ds_read_b128 v[198:201], v190 offset:17408
	ds_read_b128 v[202:205], v190 offset:18432
	ds_read_b128 v[206:209], v190 offset:19456
	ds_read_b128 v[210:213], v190 offset:20480
	ds_read_b128 v[214:217], v190 offset:21504
	ds_read_b128 v[218:221], v190 offset:22528
	ds_read_b128 v[222:225], v190 offset:23552
	global_load_lds_dwordx4 v[178:179], off
	s_add_i32 m0, s49, 0x2000
	s_add_u32 s50, s26, 0x2000
	v_lshl_add_u64 v[180:181], s[26:27], 0, v[168:169]
	s_addc_u32 s51, s27, 0
	s_add_i32 s49, s42, s30
	global_load_lds_dwordx4 v[180:181], off
	v_lshl_add_u64 v[182:183], s[50:51], 0, v[164:165]
	s_mov_b32 m0, s49
	v_lshl_add_u64 v[184:185], s[28:29], 0, v[166:167]
	global_load_lds_dwordx4 v[182:183], off
	v_lshl_add_u64 v[182:183], s[50:51], 0, v[168:169]
	s_add_i32 m0, s49, 0x2000
	s_nop 0
	global_load_lds_dwordx4 v[182:183], off
	v_lshl_add_u64 v[182:183], s[28:29], 0, v[162:163]
	s_mov_b32 m0, s23
	s_nop 0
	global_load_lds_dwordx4 v[182:183], off
	s_mov_b32 m0, s34
	s_nop 0
	global_load_lds_dwordx4 v[184:185], off
	s_waitcnt vmcnt(8)
	s_waitcnt lgkmcnt(0)
	s_barrier
	s_setprio 1
	s_nop 3
	s_waitcnt lgkmcnt(0)
	v_mfma_scale_f32_16x16x128_f8f6f4 v[94:97], v[26:33], v[194:201], v[94:97], v191, v192 op_sel_hi:[0,0,0]
	v_mfma_scale_f32_16x16x128_f8f6f4 v[90:93], v[18:25], v[194:201], v[90:93], v191, v192 op_sel_hi:[0,0,0]
	v_mfma_scale_f32_16x16x128_f8f6f4 v[78:81], v[26:33], v[202:209], v[78:81], v191, v192 op_sel_hi:[0,0,0]
	v_mfma_scale_f32_16x16x128_f8f6f4 v[74:77], v[18:25], v[202:209], v[74:77], v191, v192 op_sel_hi:[0,0,0]
	v_mfma_scale_f32_16x16x128_f8f6f4 v[62:65], v[26:33], v[210:217], v[62:65], v191, v192 op_sel_hi:[0,0,0]
	v_mfma_scale_f32_16x16x128_f8f6f4 v[58:61], v[18:25], v[210:217], v[58:61], v191, v192 op_sel_hi:[0,0,0]
	v_mfma_scale_f32_16x16x128_f8f6f4 v[46:49], v[26:33], v[218:225], v[46:49], v191, v192 op_sel_hi:[0,0,0]
	v_mfma_scale_f32_16x16x128_f8f6f4 v[42:45], v[18:25], v[218:225], v[42:45], v191, v192 op_sel_hi:[0,0,0]
	s_setprio 0
	s_setprio 1
	s_nop 3
	v_mfma_scale_f32_16x16x128_f8f6f4 v[86:89], v[10:17], v[194:201], v[86:89], v191, v192 op_sel_hi:[0,0,0]
	v_mfma_scale_f32_16x16x128_f8f6f4 v[82:85], v[2:9], v[194:201], v[82:85], v191, v192 op_sel_hi:[0,0,0]
	v_mfma_scale_f32_16x16x128_f8f6f4 v[70:73], v[10:17], v[202:209], v[70:73], v191, v192 op_sel_hi:[0,0,0]
	v_mfma_scale_f32_16x16x128_f8f6f4 v[66:69], v[2:9], v[202:209], v[66:69], v191, v192 op_sel_hi:[0,0,0]
	v_mfma_scale_f32_16x16x128_f8f6f4 v[54:57], v[10:17], v[210:217], v[54:57], v191, v192 op_sel_hi:[0,0,0]
	v_mfma_scale_f32_16x16x128_f8f6f4 v[50:53], v[2:9], v[210:217], v[50:53], v191, v192 op_sel_hi:[0,0,0]
	v_mfma_scale_f32_16x16x128_f8f6f4 v[38:41], v[10:17], v[218:225], v[38:41], v191, v192 op_sel_hi:[0,0,0]
	v_mfma_scale_f32_16x16x128_f8f6f4 v[34:37], v[2:9], v[218:225], v[34:37], v191, v192 op_sel_hi:[0,0,0]
	s_setprio 0
	s_barrier
; #define PG8_STAGE(bufoff, gbase, voff) do { _Pragma("unroll") for (int _i = 0; _i < 2; ++_i) \
;         __builtin_amdgcn_global_load_lds((const unsigned*)((const char*)(gbase) + (voff)[_i]), (PG8_LAS unsigned*)(lds + (bufoff) + ldsw + _i * 8192), 16, 0, 0); } while (0)
; #define PG8_STAGE_A(bufoff, gbase, h, nx) do { if constexpr (Sched::GATHER) { const unsigned vv_[2] = {(nx) ? vAn[h][0] : vA[h][0], (nx) ? vAn[h][1] : vA[h][1]}; PG8_STAGE(bufoff, gbase, vv_); } \
;         else { PG8_STAGE(bufoff, (gbase) + (h) * hstep, voffA); } } while (0)
; #define PG8_LDA(dst, b, h) do { _Pragma("unroll") for (int m = 0; m < 4; ++m) _Pragma("unroll") for (int k = 0; k < 2; ++k) dst[m][k] = *(const PG8_LAS bf16x8*)(lds + PG8_SA(b, h) + aoff + m * 2048 + k * 1024); } while (0)
; #define PG8_LDB(dst, b, h) do { _Pragma("unroll") for (int n = 0; n < 2; ++n) _Pragma("unroll") for (int k = 0; k < 2; ++k) dst[n][k] = *(const PG8_LAS bf16x8*)(lds + PG8_SB(b, h) + boff + n * 2048 + k * 1024); } while (0)
; #define PG8_WAIT_V(n) asm volatile("s_waitcnt vmcnt(" #n ")" ::: "memory")
; #define PG8_WAIT_L(n) asm volatile("s_waitcnt lgkmcnt(" #n ")" ::: "memory")
; #define PG8_BAR __builtin_amdgcn_s_barrier()
; #define PG8_SCHED __builtin_amdgcn_sched_barrier(0)
;     ...
;             PG8_LDB(B0, 1, 0); PG8_LDB(B1, 1, 1); PG8_SCHED; PG8_LDA(At, 1, 0); PG8_STAGE_A(PG8_SA(0, 1), a2, 1, last);
;             PG8_WAIT_V(8); PG8_WAIT_L(0); PG8_BAR; PG8_MMA(0, 0, At, B0); PG8_MMA(0, 1, At, B1); PG8_BAR; PG8_SCHED;
;             PG8_LDA(At, 1, 1); PG8_STAGE(PG8_SB(1, 0), b3, voffB); PG8_STAGE(PG8_SB(1, 1), b3 + hstepB, voffB); PG8_STAGE_A(PG8_SA(1, 0), a3, 0, last);
;             PG8_WAIT_V(8); PG8_WAIT_L(0); PG8_BAR; PG8_MMA(1, 0, At, B0); PG8_MMA(1, 1, At, B1); PG8_BAR; PG8_SCHED;
;     ...
;         if constexpr (F8) asm volatile("s_nop 15\n\ts_nop 15\n\ts_nop 15" ::: "memory");
;         if constexpr (ALIGN_EPI) { if (wr == 0) PG8_BAR; }
;         if constexpr (!Epi::AFTER_DRAIN) { E(acc, cur, wr, wc, fr, fq); S.done(cur); }
;         if (!has_next) break;
	s_add_i32 s49, 0, 0x18000
	s_add_i32 s50, 0, 0x1c000
	v_add_u32_e32 v14, s49, v186
	v_add_u32_e32 v30, s50, v186
	ds_read_b128 v[2:5], v14
	ds_read_b128 v[6:9], v14 offset:1024
	ds_read_b128 v[10:13], v14 offset:2048
	ds_read_b128 v[14:17], v14 offset:3072
	ds_read_b128 v[18:21], v30
	ds_read_b128 v[22:25], v30 offset:1024
	ds_read_b128 v[26:29], v30 offset:2048
	ds_read_b128 v[30:33], v30 offset:3072
	s_add_u32 s28, s28, 0x20000
	s_addc_u32 s29, s29, 0
	s_mov_b32 m0, s35
	v_lshl_add_u64 v[226:227], s[28:29], 0, v[162:163]
	ds_read_b128 v[194:197], v190 offset:32768
	ds_read_b128 v[198:201], v190 offset:33792
	ds_read_b128 v[202:205], v190 offset:34816
	ds_read_b128 v[206:209], v190 offset:35840
	ds_read_b128 v[210:213], v190 offset:36864
	ds_read_b128 v[214:217], v190 offset:37888
	ds_read_b128 v[218:221], v190 offset:38912
	ds_read_b128 v[222:225], v190 offset:39936
	global_load_lds_dwordx4 v[226:227], off
	v_lshl_add_u64 v[226:227], s[28:29], 0, v[166:167]
	s_mov_b32 m0, s36
	s_nop 0
	global_load_lds_dwordx4 v[226:227], off
	s_waitcnt vmcnt(8)
	s_waitcnt lgkmcnt(0)
	s_barrier
	s_setprio 1
	s_nop 3
	s_waitcnt lgkmcnt(0)
	v_mfma_scale_f32_16x16x128_f8f6f4 v[158:161], v[2:9], v[194:201], v[158:161], v191, v192 op_sel_hi:[0,0,0]
	v_mfma_scale_f32_16x16x128_f8f6f4 v[154:157], v[10:17], v[194:201], v[154:157], v191, v192 op_sel_hi:[0,0,0]
	v_mfma_scale_f32_16x16x128_f8f6f4 v[142:145], v[2:9], v[202:209], v[142:145], v191, v192 op_sel_hi:[0,0,0]
	v_mfma_scale_f32_16x16x128_f8f6f4 v[138:141], v[10:17], v[202:209], v[138:141], v191, v192 op_sel_hi:[0,0,0]
	v_mfma_scale_f32_16x16x128_f8f6f4 v[126:129], v[2:9], v[210:217], v[126:129], v191, v192 op_sel_hi:[0,0,0]
	v_mfma_scale_f32_16x16x128_f8f6f4 v[122:125], v[10:17], v[210:217], v[122:125], v191, v192 op_sel_hi:[0,0,0]
	v_mfma_scale_f32_16x16x128_f8f6f4 v[110:113], v[2:9], v[218:225], v[110:113], v191, v192 op_sel_hi:[0,0,0]
	v_mfma_scale_f32_16x16x128_f8f6f4 v[106:109], v[10:17], v[218:225], v[106:109], v191, v192 op_sel_hi:[0,0,0]
	s_setprio 0
	s_setprio 1
	s_nop 3
	v_mfma_scale_f32_16x16x128_f8f6f4 v[150:153], v[18:25], v[194:201], v[150:153], v191, v192 op_sel_hi:[0,0,0]
	v_mfma_scale_f32_16x16x128_f8f6f4 v[146:149], v[26:33], v[194:201], v[146:149], v191, v192 op_sel_hi:[0,0,0]
	v_mfma_scale_f32_16x16x128_f8f6f4 v[134:137], v[18:25], v[202:209], v[134:137], v191, v192 op_sel_hi:[0,0,0]
	v_mfma_scale_f32_16x16x128_f8f6f4 v[130:133], v[26:33], v[202:209], v[130:133], v191, v192 op_sel_hi:[0,0,0]
	v_mfma_scale_f32_16x16x128_f8f6f4 v[118:121], v[18:25], v[210:217], v[118:121], v191, v192 op_sel_hi:[0,0,0]
	v_mfma_scale_f32_16x16x128_f8f6f4 v[114:117], v[26:33], v[210:217], v[114:117], v191, v192 op_sel_hi:[0,0,0]
	v_mfma_scale_f32_16x16x128_f8f6f4 v[102:105], v[18:25], v[218:225], v[102:105], v191, v192 op_sel_hi:[0,0,0]
	v_mfma_scale_f32_16x16x128_f8f6f4 v[98:101], v[26:33], v[218:225], v[98:101], v191, v192 op_sel_hi:[0,0,0]
	s_setprio 0
	s_barrier
	s_add_i32 s28, s49, s30
	v_lshl_add_u64 v[178:179], v[178:179], 0, s[8:9]
	s_mov_b32 m0, s28
	ds_read_b128 v[194:197], v190 offset:49152
	ds_read_b128 v[198:201], v190 offset:50176
	ds_read_b128 v[202:205], v190 offset:51200
	ds_read_b128 v[206:209], v190 offset:52224
	ds_read_b128 v[210:213], v190 offset:53248
	ds_read_b128 v[214:217], v190 offset:54272
	ds_read_b128 v[218:221], v190 offset:55296
	ds_read_b128 v[222:225], v190 offset:56320
	global_load_lds_dwordx4 v[178:179], off
	s_add_i32 m0, s28, 0x2000
	s_add_u32 s26, s26, 0x2080
	v_lshl_add_u64 v[178:179], v[180:181], 0, s[8:9]
	s_addc_u32 s27, s27, 0
	s_add_i32 s28, s50, s30
	global_load_lds_dwordx4 v[178:179], off
	v_lshl_add_u64 v[178:179], s[26:27], 0, v[164:165]
	s_mov_b32 m0, s28
	s_nop 0
	global_load_lds_dwordx4 v[178:179], off
	v_lshl_add_u64 v[178:179], s[26:27], 0, v[168:169]
	s_add_i32 m0, s28, 0x2000
	s_nop 0
	global_load_lds_dwordx4 v[178:179], off
	v_lshl_add_u64 v[178:179], v[182:183], 0, s[8:9]
	s_mov_b32 m0, s39
	s_nop 0
	global_load_lds_dwordx4 v[178:179], off
	v_lshl_add_u64 v[178:179], v[184:185], 0, s[8:9]
	s_mov_b32 m0, s40
	s_nop 0
	global_load_lds_dwordx4 v[178:179], off
	s_waitcnt vmcnt(8)
	s_waitcnt lgkmcnt(0)
	s_barrier
	s_setprio 1
	s_nop 3
	s_waitcnt lgkmcnt(0)
	v_mfma_scale_f32_16x16x128_f8f6f4 v[94:97], v[2:9], v[194:201], v[94:97], v191, v192 op_sel_hi:[0,0,0]
	v_mfma_scale_f32_16x16x128_f8f6f4 v[90:93], v[10:17], v[194:201], v[90:93], v191, v192 op_sel_hi:[0,0,0]
	v_mfma_scale_f32_16x16x128_f8f6f4 v[78:81], v[2:9], v[202:209], v[78:81], v191, v192 op_sel_hi:[0,0,0]
	v_mfma_scale_f32_16x16x128_f8f6f4 v[74:77], v[10:17], v[202:209], v[74:77], v191, v192 op_sel_hi:[0,0,0]
	v_mfma_scale_f32_16x16x128_f8f6f4 v[62:65], v[2:9], v[210:217], v[62:65], v191, v192 op_sel_hi:[0,0,0]
	v_mfma_scale_f32_16x16x128_f8f6f4 v[58:61], v[10:17], v[210:217], v[58:61], v191, v192 op_sel_hi:[0,0,0]
	v_mfma_scale_f32_16x16x128_f8f6f4 v[46:49], v[2:9], v[218:225], v[46:49], v191, v192 op_sel_hi:[0,0,0]
	v_mfma_scale_f32_16x16x128_f8f6f4 v[42:45], v[10:17], v[218:225], v[42:45], v191, v192 op_sel_hi:[0,0,0]
	s_setprio 0
	s_setprio 1
	s_nop 3
	v_mfma_scale_f32_16x16x128_f8f6f4 v[86:89], v[18:25], v[194:201], v[86:89], v191, v192 op_sel_hi:[0,0,0]
	v_mfma_scale_f32_16x16x128_f8f6f4 v[82:85], v[26:33], v[194:201], v[82:85], v191, v192 op_sel_hi:[0,0,0]
	v_mfma_scale_f32_16x16x128_f8f6f4 v[70:73], v[18:25], v[202:209], v[70:73], v191, v192 op_sel_hi:[0,0,0]
	v_mfma_scale_f32_16x16x128_f8f6f4 v[66:69], v[26:33], v[202:209], v[66:69], v191, v192 op_sel_hi:[0,0,0]
	v_mfma_scale_f32_16x16x128_f8f6f4 v[54:57], v[18:25], v[210:217], v[54:57], v191, v192 op_sel_hi:[0,0,0]
	v_mfma_scale_f32_16x16x128_f8f6f4 v[50:53], v[26:33], v[210:217], v[50:53], v191, v192 op_sel_hi:[0,0,0]
	v_mfma_scale_f32_16x16x128_f8f6f4 v[38:41], v[18:25], v[218:225], v[38:41], v191, v192 op_sel_hi:[0,0,0]
	v_mfma_scale_f32_16x16x128_f8f6f4 v[34:37], v[26:33], v[218:225], v[34:37], v191, v192 op_sel_hi:[0,0,0]
	s_setprio 0
	s_barrier
	s_add_i32 s48, s48, 2
	s_add_u32 s24, s24, 0x100
	s_addc_u32 s25, s25, 0
	s_add_u32 s46, s46, 0x100
	s_addc_u32 s47, s47, 0
	s_cmp_gt_u32 s48, 5
	s_cbranch_scc0 .LBB0_1205
	s_and_b64 vcc, exec, s[10:11]
	s_cbranch_vccz .LBB0_1208
	s_barrier
; __device__ __forceinline__ unsigned cvt_pk_bf16(float lo, float hi) { unsigned r; asm volatile("v_cvt_pk_bf16_f32 %0, %1, %2" : "=v"(r) : "v"(lo), "v"(hi)); return r; }
;     __device__ __forceinline__ void operator()(const f32x4 (&acc)[2][2][4][2], const Unit& u, int wr, int wc, int fr, int fq) const {
;         const int row0 = u.pm * BM + wr * 64 + fr, col0 = u.pn * BM + wc * 64 + 16 * fq;
; #pragma unroll
;         for (int ai = 0; ai < 2; ++ai)
; #pragma unroll
;             for (int m = 0; m < 4; ++m) { const size_t off = (size_t)(row0 + ai * HALF + m * 16) * ldc + col0;
;                 f32x4 r[4];
;                 if constexpr (RESID_F32) {
; #pragma unroll
;                     for (int p = 0; p < 4; ++p) r[p] = *(const f32x4*)((const float*)resid + off + 4 * p); }
;                 else { const u32x4 w0 = *(const u32x4*)((const bf16_t*)resid + off), w1 = *(const u32x4*)((const bf16_t*)resid + off + 8);
;                     r[0] = (f32x4){__uint_as_float(w0.x << 16), __uint_as_float(w0.x & 0xffff0000u), __uint_as_float(w0.y << 16), __uint_as_float(w0.y & 0xffff0000u)};
;                     r[1] = (f32x4){__uint_as_float(w0.z << 16), __uint_as_float(w0.z & 0xffff0000u), __uint_as_float(w0.w << 16), __uint_as_float(w0.w & 0xffff0000u)};
;                     r[2] = (f32x4){__uint_as_float(w1.x << 16), __uint_as_float(w1.x & 0xffff0000u), __uint_as_float(w1.y << 16), __uint_as_float(w1.y & 0xffff0000u)};
;                     r[3] = (f32x4){__uint_as_float(w1.z << 16), __uint_as_float(w1.z & 0xffff0000u), __uint_as_float(w1.w << 16), __uint_as_float(w1.w & 0xffff0000u)}; }
;                 unsigned o[8];
; #pragma unroll
;                 for (int bj = 0; bj < 2; ++bj)
; #pragma unroll
;                     for (int n = 0; n < 2; ++n) { const f32x4 v = r[2 * bj + n] + acc[ai][bj][m][n]; o[4 * bj + 2 * n] = cvt_pk_bf16(v[0], v[1]); o[4 * bj + 2 * n + 1] = cvt_pk_bf16(v[2], v[3]); }
;                 *(u32x4*)(out + off) = (u32x4){o[0], o[1], o[2], o[3]}; *(u32x4*)(out + off + 8) = (u32x4){o[4], o[5], o[6], o[7]}; }
.LBB0_1208:
	v_lshl_add_u32 v4, s22, 8, v1
	v_lshl_or_b32 v2, s33, 8, v187
	v_readlane_b32 s24, v255, 11
	v_readlane_b32 s25, v255, 12
	v_lshl_add_u32 v178, v4, 10, v2
	v_lshlrev_b32_e32 v179, 1, v178
	s_nop 4
	global_load_dwordx4 v[2:5], v179, s[24:25]
	global_load_dwordx4 v[6:9], v179, s[24:25] offset:16
	v_add_u32_e32 v180, 0x8000, v179
	global_load_dwordx4 v[10:13], v180, s[24:25]
	global_load_dwordx4 v[14:17], v180, s[24:25] offset:16
	v_add_u32_e32 v180, 0x10000, v179
	global_load_dwordx4 v[18:21], v180, s[24:25]
	global_load_dwordx4 v[22:25], v180, s[24:25] offset:16
	v_add_u32_e32 v180, 0x18000, v179
	global_load_dwordx4 v[26:29], v180, s[24:25]
	global_load_dwordx4 v[30:33], v180, s[24:25] offset:16
	v_add_u32_e32 v180, 0x40000, v179
	global_load_dwordx4 v[194:197], v180, s[24:25]
	global_load_dwordx4 v[198:201], v180, s[24:25] offset:16
	v_add_u32_e32 v180, 0x48000, v179
	global_load_dwordx4 v[202:205], v180, s[24:25]
	global_load_dwordx4 v[206:209], v180, s[24:25] offset:16
	v_add_u32_e32 v180, 0x50000, v179
	global_load_dwordx4 v[210:213], v180, s[24:25]
	global_load_dwordx4 v[214:217], v180, s[24:25] offset:16
	v_add_u32_e32 v180, 0x58000, v179
	global_load_dwordx4 v[218:221], v180, s[24:25]
	global_load_dwordx4 v[222:225], v180, s[24:25] offset:16
	s_waitcnt vmcnt(14)
	v_lshlrev_b32_e32 v228, 16, v2
	v_and_b32_e32 v229, 0xffff0000, v2
	v_lshlrev_b32_e32 v230, 16, v3
	v_and_b32_e32 v231, 0xffff0000, v3
	v_lshlrev_b32_e32 v232, 16, v4
	v_and_b32_e32 v233, 0xffff0000, v4
	v_lshlrev_b32_e32 v234, 16, v5
	v_and_b32_e32 v235, 0xffff0000, v5
	v_lshlrev_b32_e32 v236, 16, v6
	v_and_b32_e32 v237, 0xffff0000, v6
	v_lshlrev_b32_e32 v238, 16, v7
	v_and_b32_e32 v239, 0xffff0000, v7
	v_lshlrev_b32_e32 v240, 16, v8
	v_and_b32_e32 v241, 0xffff0000, v8
	v_lshlrev_b32_e32 v242, 16, v9
	v_and_b32_e32 v243, 0xffff0000, v9
	v_pk_add_f32 v[228:229], v[158:159], v[228:229]
	v_pk_add_f32 v[230:231], v[160:161], v[230:231]
	v_pk_add_f32 v[232:233], v[154:155], v[232:233]
	v_pk_add_f32 v[234:235], v[156:157], v[234:235]
	v_pk_add_f32 v[236:237], v[150:151], v[236:237]
	v_pk_add_f32 v[238:239], v[152:153], v[238:239]
	v_pk_add_f32 v[240:241], v[146:147], v[240:241]
	v_pk_add_f32 v[242:243], v[148:149], v[242:243]
	v_cvt_pk_bf16_f32 v2, v228, v229
	v_cvt_pk_bf16_f32 v3, v230, v231
	v_cvt_pk_bf16_f32 v4, v232, v233
	v_cvt_pk_bf16_f32 v5, v234, v235
	v_cvt_pk_bf16_f32 v6, v236, v237
	v_cvt_pk_bf16_f32 v7, v238, v239
	v_cvt_pk_bf16_f32 v8, v240, v241
	v_cvt_pk_bf16_f32 v9, v242, v243
	global_store_dwordx4 v179, v[2:5], s[24:25]
	global_store_dwordx4 v179, v[6:9], s[24:25] offset:16
	s_waitcnt vmcnt(14)
	v_lshlrev_b32_e32 v228, 16, v10
	v_and_b32_e32 v229, 0xffff0000, v10
	v_lshlrev_b32_e32 v230, 16, v11
	v_and_b32_e32 v231, 0xffff0000, v11
	v_lshlrev_b32_e32 v232, 16, v12
	v_and_b32_e32 v233, 0xffff0000, v12
	v_lshlrev_b32_e32 v234, 16, v13
	v_and_b32_e32 v235, 0xffff0000, v13
	v_lshlrev_b32_e32 v236, 16, v14
	v_and_b32_e32 v237, 0xffff0000, v14
	v_lshlrev_b32_e32 v238, 16, v15
	v_and_b32_e32 v239, 0xffff0000, v15
	v_lshlrev_b32_e32 v240, 16, v16
	v_and_b32_e32 v241, 0xffff0000, v16
	v_lshlrev_b32_e32 v242, 16, v17
	v_and_b32_e32 v243, 0xffff0000, v17
	v_pk_add_f32 v[228:229], v[142:143], v[228:229]
	v_pk_add_f32 v[230:231], v[144:145], v[230:231]
	v_pk_add_f32 v[232:233], v[138:139], v[232:233]
	v_pk_add_f32 v[234:235], v[140:141], v[234:235]
	v_pk_add_f32 v[236:237], v[134:135], v[236:237]
	v_pk_add_f32 v[238:239], v[136:137], v[238:239]
	v_pk_add_f32 v[240:241], v[130:131], v[240:241]
	v_pk_add_f32 v[242:243], v[132:133], v[242:243]
	v_cvt_pk_bf16_f32 v10, v228, v229
	v_cvt_pk_bf16_f32 v11, v230, v231
	v_cvt_pk_bf16_f32 v12, v232, v233
	v_cvt_pk_bf16_f32 v13, v234, v235
	v_cvt_pk_bf16_f32 v14, v236, v237
	v_cvt_pk_bf16_f32 v15, v238, v239
	v_cvt_pk_bf16_f32 v16, v240, v241
	v_cvt_pk_bf16_f32 v17, v242, v243
	v_add_u32_e32 v181, 0x8000, v179
	global_store_dwordx4 v181, v[10:13], s[24:25]
	global_store_dwordx4 v181, v[14:17], s[24:25] offset:16
	s_waitcnt vmcnt(14)
	v_lshlrev_b32_e32 v228, 16, v18
	v_and_b32_e32 v229, 0xffff0000, v18
	v_lshlrev_b32_e32 v230, 16, v19
	v_and_b32_e32 v231, 0xffff0000, v19
	v_lshlrev_b32_e32 v232, 16, v20
	v_and_b32_e32 v233, 0xffff0000, v20
	v_lshlrev_b32_e32 v234, 16, v21
	v_and_b32_e32 v235, 0xffff0000, v21
	v_lshlrev_b32_e32 v236, 16, v22
	v_and_b32_e32 v237, 0xffff0000, v22
	v_lshlrev_b32_e32 v238, 16, v23
	v_and_b32_e32 v239, 0xffff0000, v23
	v_lshlrev_b32_e32 v240, 16, v24
	v_and_b32_e32 v241, 0xffff0000, v24
	v_lshlrev_b32_e32 v242, 16, v25
	v_and_b32_e32 v243, 0xffff0000, v25
	v_pk_add_f32 v[228:229], v[126:127], v[228:229]
	v_pk_add_f32 v[230:231], v[128:129], v[230:231]
	v_pk_add_f32 v[232:233], v[122:123], v[232:233]
	v_pk_add_f32 v[234:235], v[124:125], v[234:235]
	v_pk_add_f32 v[236:237], v[118:119], v[236:237]
	v_pk_add_f32 v[238:239], v[120:121], v[238:239]
	v_pk_add_f32 v[240:241], v[114:115], v[240:241]
	v_pk_add_f32 v[242:243], v[116:117], v[242:243]
	v_cvt_pk_bf16_f32 v18, v228, v229
	v_cvt_pk_bf16_f32 v19, v230, v231
	v_cvt_pk_bf16_f32 v20, v232, v233
	v_cvt_pk_bf16_f32 v21, v234, v235
	v_cvt_pk_bf16_f32 v22, v236, v237
	v_cvt_pk_bf16_f32 v23, v238, v239
	v_cvt_pk_bf16_f32 v24, v240, v241
	v_cvt_pk_bf16_f32 v25, v242, v243
	v_add_u32_e32 v181, 0x10000, v179
	global_store_dwordx4 v181, v[18:21], s[24:25]
	global_store_dwordx4 v181, v[22:25], s[24:25] offset:16
	s_waitcnt vmcnt(14)
; __device__ __forceinline__ unsigned cvt_pk_bf16(float lo, float hi) { unsigned r; asm volatile("v_cvt_pk_bf16_f32 %0, %1, %2" : "=v"(r) : "v"(lo), "v"(hi)); return r; }
;     __device__ __forceinline__ void operator()(const f32x4 (&acc)[2][2][4][2], const Unit& u, int wr, int wc, int fr, int fq) const {
;     ...
;         for (int ai = 0; ai < 2; ++ai)
; #pragma unroll
;             for (int m = 0; m < 4; ++m) { const size_t off = (size_t)(row0 + ai * HALF + m * 16) * ldc + col0;
;                 f32x4 r[4];
;                 if constexpr (RESID_F32) {
; #pragma unroll
;                     for (int p = 0; p < 4; ++p) r[p] = *(const f32x4*)((const float*)resid + off + 4 * p); }
;                 else { const u32x4 w0 = *(const u32x4*)((const bf16_t*)resid + off), w1 = *(const u32x4*)((const bf16_t*)resid + off + 8);
;                     r[0] = (f32x4){__uint_as_float(w0.x << 16), __uint_as_float(w0.x & 0xffff0000u), __uint_as_float(w0.y << 16), __uint_as_float(w0.y & 0xffff0000u)};
;                     r[1] = (f32x4){__uint_as_float(w0.z << 16), __uint_as_float(w0.z & 0xffff0000u), __uint_as_float(w0.w << 16), __uint_as_float(w0.w & 0xffff0000u)};
;                     r[2] = (f32x4){__uint_as_float(w1.x << 16), __uint_as_float(w1.x & 0xffff0000u), __uint_as_float(w1.y << 16), __uint_as_float(w1.y & 0xffff0000u)};
;                     r[3] = (f32x4){__uint_as_float(w1.z << 16), __uint_as_float(w1.z & 0xffff0000u), __uint_as_float(w1.w << 16), __uint_as_float(w1.w & 0xffff0000u)}; }
;                 unsigned o[8];
; #pragma unroll
;                 for (int bj = 0; bj < 2; ++bj)
; #pragma unroll
;                     for (int n = 0; n < 2; ++n) { const f32x4 v = r[2 * bj + n] + acc[ai][bj][m][n]; o[4 * bj + 2 * n] = cvt_pk_bf16(v[0], v[1]); o[4 * bj + 2 * n + 1] = cvt_pk_bf16(v[2], v[3]); }
;                 *(u32x4*)(out + off) = (u32x4){o[0], o[1], o[2], o[3]}; *(u32x4*)(out + off + 8) = (u32x4){o[4], o[5], o[6], o[7]}; }
	v_lshlrev_b32_e32 v228, 16, v26
	v_and_b32_e32 v229, 0xffff0000, v26
	v_lshlrev_b32_e32 v230, 16, v27
	v_and_b32_e32 v231, 0xffff0000, v27
	v_lshlrev_b32_e32 v232, 16, v28
	v_and_b32_e32 v233, 0xffff0000, v28
	v_lshlrev_b32_e32 v234, 16, v29
	v_and_b32_e32 v235, 0xffff0000, v29
	v_lshlrev_b32_e32 v236, 16, v30
	v_and_b32_e32 v237, 0xffff0000, v30
	v_lshlrev_b32_e32 v238, 16, v31
	v_and_b32_e32 v239, 0xffff0000, v31
	v_lshlrev_b32_e32 v240, 16, v32
	v_and_b32_e32 v241, 0xffff0000, v32
	v_lshlrev_b32_e32 v242, 16, v33
	v_and_b32_e32 v243, 0xffff0000, v33
	v_pk_add_f32 v[228:229], v[110:111], v[228:229]
	v_pk_add_f32 v[230:231], v[112:113], v[230:231]
	v_pk_add_f32 v[232:233], v[106:107], v[232:233]
	v_pk_add_f32 v[234:235], v[108:109], v[234:235]
	v_pk_add_f32 v[236:237], v[102:103], v[236:237]
	v_pk_add_f32 v[238:239], v[104:105], v[238:239]
	v_pk_add_f32 v[240:241], v[98:99], v[240:241]
	v_pk_add_f32 v[242:243], v[100:101], v[242:243]
	v_cvt_pk_bf16_f32 v26, v228, v229
	v_cvt_pk_bf16_f32 v27, v230, v231
	v_cvt_pk_bf16_f32 v28, v232, v233
	v_cvt_pk_bf16_f32 v29, v234, v235
	v_cvt_pk_bf16_f32 v30, v236, v237
	v_cvt_pk_bf16_f32 v31, v238, v239
	v_cvt_pk_bf16_f32 v32, v240, v241
	v_cvt_pk_bf16_f32 v33, v242, v243
	v_add_u32_e32 v181, 0x18000, v179
	global_store_dwordx4 v181, v[26:29], s[24:25]
	global_store_dwordx4 v181, v[30:33], s[24:25] offset:16
	s_waitcnt vmcnt(14)
	v_lshlrev_b32_e32 v228, 16, v194
	v_and_b32_e32 v229, 0xffff0000, v194
	v_lshlrev_b32_e32 v230, 16, v195
	v_and_b32_e32 v231, 0xffff0000, v195
	v_lshlrev_b32_e32 v232, 16, v196
	v_and_b32_e32 v233, 0xffff0000, v196
	v_lshlrev_b32_e32 v234, 16, v197
	v_and_b32_e32 v235, 0xffff0000, v197
	v_lshlrev_b32_e32 v236, 16, v198
	v_and_b32_e32 v237, 0xffff0000, v198
	v_lshlrev_b32_e32 v238, 16, v199
	v_and_b32_e32 v239, 0xffff0000, v199
	v_lshlrev_b32_e32 v240, 16, v200
	v_and_b32_e32 v241, 0xffff0000, v200
	v_lshlrev_b32_e32 v242, 16, v201
	v_and_b32_e32 v243, 0xffff0000, v201
	v_pk_add_f32 v[228:229], v[94:95], v[228:229]
	v_pk_add_f32 v[230:231], v[96:97], v[230:231]
	v_pk_add_f32 v[232:233], v[90:91], v[232:233]
	v_pk_add_f32 v[234:235], v[92:93], v[234:235]
	v_pk_add_f32 v[236:237], v[86:87], v[236:237]
	v_pk_add_f32 v[238:239], v[88:89], v[238:239]
	v_pk_add_f32 v[240:241], v[82:83], v[240:241]
	v_pk_add_f32 v[242:243], v[84:85], v[242:243]
	v_cvt_pk_bf16_f32 v194, v228, v229
	v_cvt_pk_bf16_f32 v195, v230, v231
	v_cvt_pk_bf16_f32 v196, v232, v233
	v_cvt_pk_bf16_f32 v197, v234, v235
	v_cvt_pk_bf16_f32 v198, v236, v237
	v_cvt_pk_bf16_f32 v199, v238, v239
	v_cvt_pk_bf16_f32 v200, v240, v241
	v_cvt_pk_bf16_f32 v201, v242, v243
	v_add_u32_e32 v181, 0x40000, v179
	global_store_dwordx4 v181, v[194:197], s[24:25]
	global_store_dwordx4 v181, v[198:201], s[24:25] offset:16
	s_waitcnt vmcnt(14)
	v_lshlrev_b32_e32 v228, 16, v202
	v_and_b32_e32 v229, 0xffff0000, v202
	v_lshlrev_b32_e32 v230, 16, v203
	v_and_b32_e32 v231, 0xffff0000, v203
	v_lshlrev_b32_e32 v232, 16, v204
	v_and_b32_e32 v233, 0xffff0000, v204
	v_lshlrev_b32_e32 v234, 16, v205
	v_and_b32_e32 v235, 0xffff0000, v205
	v_lshlrev_b32_e32 v236, 16, v206
	v_and_b32_e32 v237, 0xffff0000, v206
	v_lshlrev_b32_e32 v238, 16, v207
	v_and_b32_e32 v239, 0xffff0000, v207
	v_lshlrev_b32_e32 v240, 16, v208
	v_and_b32_e32 v241, 0xffff0000, v208
	v_lshlrev_b32_e32 v242, 16, v209
	v_and_b32_e32 v243, 0xffff0000, v209
	v_pk_add_f32 v[228:229], v[78:79], v[228:229]
	v_pk_add_f32 v[230:231], v[80:81], v[230:231]
	v_pk_add_f32 v[232:233], v[74:75], v[232:233]
	v_pk_add_f32 v[234:235], v[76:77], v[234:235]
	v_pk_add_f32 v[236:237], v[70:71], v[236:237]
	v_pk_add_f32 v[238:239], v[72:73], v[238:239]
	v_pk_add_f32 v[240:241], v[66:67], v[240:241]
	v_pk_add_f32 v[242:243], v[68:69], v[242:243]
	v_cvt_pk_bf16_f32 v202, v228, v229
	v_cvt_pk_bf16_f32 v203, v230, v231
	v_cvt_pk_bf16_f32 v204, v232, v233
	v_cvt_pk_bf16_f32 v205, v234, v235
	v_cvt_pk_bf16_f32 v206, v236, v237
	v_cvt_pk_bf16_f32 v207, v238, v239
	v_cvt_pk_bf16_f32 v208, v240, v241
	v_cvt_pk_bf16_f32 v209, v242, v243
	v_add_u32_e32 v181, 0x48000, v179
	global_store_dwordx4 v181, v[202:205], s[24:25]
	global_store_dwordx4 v181, v[206:209], s[24:25] offset:16
	s_waitcnt vmcnt(14)
;     ...
;         if constexpr (!Epi::AFTER_DRAIN) { E(acc, cur, wr, wc, fr, fq); S.done(cur); }
;         if (!has_next) break;
; #pragma unroll
;         for (int a = 0; a < 2; ++a)
; #pragma unroll
;             for (int b = 0; b < 2; ++b)
; #pragma unroll
;                 for (int m = 0; m < 4; ++m)
; #pragma unroll
;                     for (int n = 0; n < 2; ++n) acc[a][b][m][n] = (f32x4){0.f, 0.f, 0.f, 0.f};
;         cur = nxt; cA = nA; cB = nB; ++ui;
;         if constexpr (Sched::GATHER) { _Pragma("unroll") for (int h_ = 0; h_ < 2; ++h_) _Pragma("unroll") for (int i_ = 0; i_ < 2; ++i_) vA[h_][i_] = vAn[h_][i_]; }
;     __device__ __forceinline__ void operator()(const f32x4 (&acc)[2][2][4][2], const Unit& u, int wr, int wc, int fr, int fq) const {
;     ...
;             for (int m = 0; m < 4; ++m) { const size_t off = (size_t)(row0 + ai * HALF + m * 16) * ldc + col0;
;                 f32x4 r[4];
;                 if constexpr (RESID_F32) {
; #pragma unroll
;                     for (int p = 0; p < 4; ++p) r[p] = *(const f32x4*)((const float*)resid + off + 4 * p); }
;                 else { const u32x4 w0 = *(const u32x4*)((const bf16_t*)resid + off), w1 = *(const u32x4*)((const bf16_t*)resid + off + 8);
;                     r[0] = (f32x4){__uint_as_float(w0.x << 16), __uint_as_float(w0.x & 0xffff0000u), __uint_as_float(w0.y << 16), __uint_as_float(w0.y & 0xffff0000u)};
;                     r[1] = (f32x4){__uint_as_float(w0.z << 16), __uint_as_float(w0.z & 0xffff0000u), __uint_as_float(w0.w << 16), __uint_as_float(w0.w & 0xffff0000u)};
;                     r[2] = (f32x4){__uint_as_float(w1.x << 16), __uint_as_float(w1.x & 0xffff0000u), __uint_as_float(w1.y << 16), __uint_as_float(w1.y & 0xffff0000u)};
;                     r[3] = (f32x4){__uint_as_float(w1.z << 16), __uint_as_float(w1.z & 0xffff0000u), __uint_as_float(w1.w << 16), __uint_as_float(w1.w & 0xffff0000u)}; }
;                 unsigned o[8];
; #pragma unroll
;                 for (int bj = 0; bj < 2; ++bj)
; #pragma unroll
;                     for (int n = 0; n < 2; ++n) { const f32x4 v = r[2 * bj + n] + acc[ai][bj][m][n]; o[4 * bj + 2 * n] = cvt_pk_bf16(v[0], v[1]); o[4 * bj + 2 * n + 1] = cvt_pk_bf16(v[2], v[3]); }
;                 *(u32x4*)(out + off) = (u32x4){o[0], o[1], o[2], o[3]}; *(u32x4*)(out + off + 8) = (u32x4){o[4], o[5], o[6], o[7]}; }
	v_lshlrev_b32_e32 v228, 16, v210
	v_and_b32_e32 v229, 0xffff0000, v210
	v_lshlrev_b32_e32 v230, 16, v211
	v_and_b32_e32 v231, 0xffff0000, v211
	v_lshlrev_b32_e32 v232, 16, v212
	v_and_b32_e32 v233, 0xffff0000, v212
	v_lshlrev_b32_e32 v234, 16, v213
	v_and_b32_e32 v235, 0xffff0000, v213
	v_lshlrev_b32_e32 v236, 16, v214
	v_and_b32_e32 v237, 0xffff0000, v214
	v_lshlrev_b32_e32 v238, 16, v215
	v_and_b32_e32 v239, 0xffff0000, v215
	v_lshlrev_b32_e32 v240, 16, v216
	v_and_b32_e32 v241, 0xffff0000, v216
	v_lshlrev_b32_e32 v242, 16, v217
	v_and_b32_e32 v243, 0xffff0000, v217
	v_pk_add_f32 v[228:229], v[62:63], v[228:229]
	v_pk_add_f32 v[230:231], v[64:65], v[230:231]
	v_pk_add_f32 v[232:233], v[58:59], v[232:233]
	v_pk_add_f32 v[234:235], v[60:61], v[234:235]
	v_pk_add_f32 v[236:237], v[54:55], v[236:237]
	v_pk_add_f32 v[238:239], v[56:57], v[238:239]
	v_pk_add_f32 v[240:241], v[50:51], v[240:241]
	v_pk_add_f32 v[242:243], v[52:53], v[242:243]
	v_cvt_pk_bf16_f32 v210, v228, v229
	v_cvt_pk_bf16_f32 v211, v230, v231
	v_cvt_pk_bf16_f32 v212, v232, v233
	v_cvt_pk_bf16_f32 v213, v234, v235
	v_cvt_pk_bf16_f32 v214, v236, v237
	v_cvt_pk_bf16_f32 v215, v238, v239
	v_cvt_pk_bf16_f32 v216, v240, v241
	v_cvt_pk_bf16_f32 v217, v242, v243
	v_add_u32_e32 v181, 0x50000, v179
	global_store_dwordx4 v181, v[210:213], s[24:25]
	global_store_dwordx4 v181, v[214:217], s[24:25] offset:16
	s_waitcnt vmcnt(14)
	v_lshlrev_b32_e32 v228, 16, v218
	v_and_b32_e32 v229, 0xffff0000, v218
	v_lshlrev_b32_e32 v230, 16, v219
	v_and_b32_e32 v231, 0xffff0000, v219
	v_lshlrev_b32_e32 v232, 16, v220
	v_and_b32_e32 v233, 0xffff0000, v220
	v_lshlrev_b32_e32 v234, 16, v221
	v_and_b32_e32 v235, 0xffff0000, v221
	v_lshlrev_b32_e32 v236, 16, v222
	v_and_b32_e32 v237, 0xffff0000, v222
	v_lshlrev_b32_e32 v238, 16, v223
	v_and_b32_e32 v239, 0xffff0000, v223
	v_lshlrev_b32_e32 v240, 16, v224
	v_and_b32_e32 v241, 0xffff0000, v224
	v_lshlrev_b32_e32 v242, 16, v225
	v_and_b32_e32 v243, 0xffff0000, v225
	v_pk_add_f32 v[228:229], v[46:47], v[228:229]
	v_pk_add_f32 v[230:231], v[48:49], v[230:231]
	v_pk_add_f32 v[232:233], v[42:43], v[232:233]
	v_pk_add_f32 v[234:235], v[44:45], v[234:235]
	v_pk_add_f32 v[236:237], v[38:39], v[236:237]
	v_pk_add_f32 v[238:239], v[40:41], v[238:239]
	v_pk_add_f32 v[240:241], v[34:35], v[240:241]
	v_pk_add_f32 v[242:243], v[36:37], v[242:243]
	v_cvt_pk_bf16_f32 v218, v228, v229
	v_cvt_pk_bf16_f32 v219, v230, v231
	v_cvt_pk_bf16_f32 v220, v232, v233
	v_cvt_pk_bf16_f32 v221, v234, v235
	v_cvt_pk_bf16_f32 v222, v236, v237
	v_cvt_pk_bf16_f32 v223, v238, v239
	v_cvt_pk_bf16_f32 v224, v240, v241
	v_cvt_pk_bf16_f32 v225, v242, v243
	v_add_u32_e32 v181, 0x58000, v179
	global_store_dwordx4 v181, v[218:221], s[24:25]
	global_store_dwordx4 v181, v[222:225], s[24:25] offset:16
	s_mov_b32 s15, 0x40000
	s_mov_b64 s[24:25], 0x40000
	s_mov_b32 s15, 0x48000
	s_mov_b64 s[24:25], 0x48000
	s_mov_b32 s15, 0x50000
	s_mov_b64 s[24:25], 0x50000
	s_andn2_b64 vcc, exec, s[2:3]
	s_mov_b64 s[2:3], -1
	s_cbranch_vccnz .LBB0_1197
	s_andn2_b64 vcc, exec, s[6:7]
	s_cbranch_vccnz .LBB0_1196
	s_barrier
	s_branch .LBB0_1196
